# rider decode only every 4th trip in the differential-attention loops (the 3 following tiles step the load base by 32 rows and the store offset by 32 B), decode block contiguous before the rider memory
# speedup vs baseline: 1.0100x; 1.0100x over previous
; DI void attn_unit_d8(unsigned char* lds, const AttnArgs& a) {
;     ...
;     auto gload = [&](int t, u32x2& kreg, u32x2& vreg) __attribute__((always_inline)) {
;         const unsigned char* kp = (t < 64) ? a.klat8 + (size_t)(t * 64 + lrow) * 256 : a.kctx8 + (size_t)((t - 64) * 64 + lrow) * 256;
;         kreg = *(const u32x2*)(kp + 8 * lch);
;         vreg = *(const u32x2*)(vsrc + (size_t)t * 64);
;     };
;     auto lstore = [&](int slot, const u32x2& kreg, const u32x2& vreg) __attribute__((always_inline)) { unsigned char* b = lds + slot * D8_SLOT;
;         *(u32x2*)(b + ldst) = kreg; *(unsigned*)(b + ldv) = vreg.x; *(unsigned*)(b + ldv + 32) = vreg.y; };
;     auto rd32 = [&](const unsigned char* p) __attribute__((always_inline)) -> v8i { const u32x4 lo = *(const u32x4*)p, hi = *(const u32x4*)(p + 16);
;         return (v8i){(int)lo.x, (int)lo.y, (int)lo.z, (int)lo.w, (int)hi.x, (int)hi.y, (int)hi.z, (int)hi.w}; };
;     auto expsum = [&](f32x16& sc, f32x4& l) __attribute__((always_inline)) {
; #pragma unroll
;         for (int i = 0; i < 16; ++i) sc[i] = __builtin_amdgcn_exp2f(sc[i]);
; #pragma unroll
;         for (int i = 0; i < 4; ++i) l += (f32x4){sc[4 * i], sc[4 * i + 1], sc[4 * i + 2], sc[4 * i + 3]};
;     };
;     auto pack8 = [&](const f32x16& s0, const f32x16& s1) __attribute__((always_inline)) -> v8i { v8i p;
; #pragma unroll
;         for (int g = 0; g < 4; ++g) { p[g] = (int)pk4_fp8_div16(s0[4 * g], s0[4 * g + 1], s0[4 * g + 2], s0[4 * g + 3]); p[4 + g] = (int)pk4_fp8_div16(s1[4 * g], s1[4 * g + 1], s1[4 * g + 2], s1[4 * g + 3]); }
;         return p; };
;     auto pack4 = [&](const f32x16& sc, v8i& p, const int o) __attribute__((always_inline)) {
; #pragma unroll
;         for (int g = 0; g < 4; ++g) p[o + g] = (int)pk4_fp8_div16(sc[4 * g], sc[4 * g + 1], sc[4 * g + 2], sc[4 * g + 3]); };
;     auto qk = [&](const unsigned char* Kb, int hh, f32x16& sa, f32x16& sb) __attribute__((always_inline)) { const v8i kf = rd32(Kb + koff + hh * 32 * A8_PITCH);
;         sa = mfma8(kf, qfa, (f32x16){}); sb = mfma8(kf, qfb, (f32x16){}); };
;     gload(a.t0, kreg0, vreg0); gload(a.t0 + 1, kreg1, vreg1); lstore(0, kreg0, vreg0); lstore(1, kreg1, vreg1);
;     gload(a.t0 + 2, kreg0, vreg0); lstore(2, kreg0, vreg0);
;     __syncthreads();
;     asm volatile("" : "+v"(qfa), "+v"(qfb));
;     f32x16 s0a, s0b, s1a, s1b;
;     qk(lds, 0, s0a, s0b);
.LBB0_663:
	s_cmp_gt_i32 s16, 3
	s_cselect_b32 s17, -4, 1
	s_add_i32 s18, s17, s16
	s_mul_i32 s6, s16, 0x2800
	s_cmp_gt_i32 s16, 2
	v_mfma_f32_32x32x64_f8f6f4 v[50:65], v[154:161], v[138:145], v[50:65]
	v_exp_f32_e32 v192, v90
	v_add_u32_e32 v90, s6, v218
	s_cselect_b32 s6, -3, 2
	s_add_i32 s6, s6, s16
	s_cmp_gt_i32 s16, 1
	s_cselect_b32 s19, -2, 3
	s_add_i32 s19, s19, s16
	s_cmp_gt_i32 s16, 0
	s_cselect_b32 s49, -1, 4
	s_min_u32 s54, s46, 64
	s_add_i32 s49, s49, s16
	s_cmp_lt_u32 s46, 61
	s_mul_i32 s17, s6, 0x2800
	s_mov_b32 s16, s6
	s_cselect_b64 s[52:53], -1, 0
	s_lshl_b32 s6, s54, 6
	s_add_i32 s54, s6, 0xc0
	s_add_i32 s55, s6, 0xfffff0c0
	s_and_b64 s[52:53], s[52:53], exec
	v_lshl_add_u64 v[98:99], v[182:183], 0, s[6:7]
	s_cselect_b32 s6, s54, s55
	s_cselect_b32 s53, s21, s48
	s_cselect_b32 s52, s20, s47
	s_min_u32 s56, s46, 63
	v_exp_f32_e32 v198, v82
	v_exp_f32_e32 v199, v83
	v_exp_f32_e32 v196, v84
	v_exp_f32_e32 v197, v85
	v_exp_f32_e32 v200, v86
	v_exp_f32_e32 v201, v87
	v_exp_f32_e32 v194, v88
	v_exp_f32_e32 v195, v89
	ds_read_b128 v[82:85], v90 offset:2560
	ds_read_b128 v[86:89], v90 offset:2576
	global_load_dwordx2 v[202:203], v[98:99], off offset:192
	v_add_u32_e32 v98, s6, v215
	s_cmp_lt_u32 s46, 60
	v_ashrrev_i32_e32 v99, 31, v98
	s_cselect_b64 s[54:55], -1, 0
	s_lshl_b32 s6, s56, 6
	v_lshlrev_b64 v[98:99], 8, v[98:99]
	s_add_i32 s56, s6, 0x100
	s_add_i32 s57, s6, 0xfffff100
	v_lshl_add_u64 v[98:99], s[52:53], 0, v[98:99]
	s_and_b64 s[52:53], s[54:55], exec
	s_cselect_b32 s54, s56, s57
	v_lshl_add_u64 v[220:221], v[98:99], 0, v[178:179]
	v_add_u32_e32 v98, s54, v215
	v_ashrrev_i32_e32 v99, 31, v98
	s_cselect_b32 s53, s21, s48
	s_cselect_b32 s52, s20, s47
	v_lshlrev_b64 v[98:99], 8, v[98:99]
	v_lshl_add_u64 v[100:101], v[182:183], 0, s[6:7]
	v_lshl_add_u64 v[98:99], s[52:53], 0, v[98:99]
	global_load_dwordx2 v[204:205], v[100:101], off offset:256
	v_lshl_add_u64 v[222:223], v[98:99], 0, v[178:179]
	s_waitcnt lgkmcnt(0)
	v_mfma_f32_32x32x64_f8f6f4 v[98:113], v[82:89], v[114:121], 0
	v_exp_f32_e32 v193, v91
	v_exp_f32_e32 v224, v92
	v_exp_f32_e32 v225, v93
	v_exp_f32_e32 v226, v94
	v_exp_f32_e32 v227, v95
	v_exp_f32_e32 v228, v96
	v_exp_f32_e32 v229, v97
	ds_read_b128 v[170:173], v90 offset:5120
	ds_read_b128 v[174:177], v90 offset:5136
	ds_read_b128 v[162:165], v90 offset:7680
	ds_read_b128 v[166:169], v90 offset:7696
	v_pk_add_f32 v[90:91], v[186:187], v[198:199]
	v_pk_add_f32 v[92:93], v[184:185], v[196:197]
	v_pk_add_f32 v[90:91], v[200:201], v[90:91]
	v_pk_add_f32 v[92:93], v[194:195], v[92:93]
	v_pk_add_f32 v[90:91], v[192:193], v[90:91]
	v_pk_add_f32 v[92:93], v[224:225], v[92:93]
	v_exp_f32_e32 v66, v66
	v_exp_f32_e32 v67, v67
	v_exp_f32_e32 v68, v68
	v_exp_f32_e32 v69, v69
	v_exp_f32_e32 v70, v70
	v_exp_f32_e32 v71, v71
	v_exp_f32_e32 v72, v72
	v_pk_add_f32 v[230:231], v[228:229], v[92:93]
	v_pk_add_f32 v[232:233], v[226:227], v[90:91]
	v_mfma_f32_32x32x64_f8f6f4 v[82:97], v[82:89], v[122:129], 0
	v_exp_f32_e32 v73, v73
	v_exp_f32_e32 v74, v74
	v_exp_f32_e32 v75, v75
	v_exp_f32_e32 v76, v76
	v_exp_f32_e32 v77, v77
	v_exp_f32_e32 v78, v78
	v_exp_f32_e32 v79, v79
	v_exp_f32_e32 v80, v80
	v_exp_f32_e32 v81, v81
	v_pk_add_f32 v[186:187], v[190:191], v[66:67]
	v_pk_add_f32 v[188:189], v[188:189], v[68:69]
	v_pk_add_f32 v[186:187], v[70:71], v[186:187]
	v_pk_add_f32 v[188:189], v[72:73], v[188:189]
	v_cvt_scalef32_pk_fp8_f32 v184, v198, v199, s36
	v_pk_add_f32 v[186:187], v[74:75], v[186:187]
	v_pk_add_f32 v[188:189], v[76:77], v[188:189]
	v_cvt_scalef32_pk_fp8_f32 v185, v200, v201, s36
	v_cvt_scalef32_pk_fp8_f32 v184, v196, v197, s36 op_sel:[0,0,0,1]
	v_pk_add_f32 v[190:191], v[78:79], v[186:187]
	v_pk_add_f32 v[188:189], v[80:81], v[188:189]
	v_mfma_f32_32x32x64_f8f6f4 v[2:17], v[154:161], v[130:137], v[2:17]
	s_mulk_i32 s18, 0x2800
	v_cvt_scalef32_pk_fp8_f32 v186, v192, v193, s36
	v_cvt_scalef32_pk_fp8_f32 v187, v226, v227, s36
	v_cvt_scalef32_pk_fp8_f32 v154, v66, v67, s36
	v_cvt_scalef32_pk_fp8_f32 v155, v70, v71, s36
	v_cvt_scalef32_pk_fp8_f32 v156, v74, v75, s36
	v_cvt_scalef32_pk_fp8_f32 v157, v78, v79, s36
	v_cvt_scalef32_pk_fp8_f32 v185, v194, v195, s36 op_sel:[0,0,0,1]
	v_add_u32_e32 v219, s18, v218
	v_cvt_scalef32_pk_fp8_f32 v186, v224, v225, s36 op_sel:[0,0,0,1]
	v_cvt_scalef32_pk_fp8_f32 v187, v228, v229, s36 op_sel:[0,0,0,1]
	v_cvt_scalef32_pk_fp8_f32 v154, v68, v69, s36 op_sel:[0,0,0,1]
	v_cvt_scalef32_pk_fp8_f32 v155, v72, v73, s36 op_sel:[0,0,0,1]
	v_cvt_scalef32_pk_fp8_f32 v156, v76, v77, s36 op_sel:[0,0,0,1]
	v_cvt_scalef32_pk_fp8_f32 v157, v80, v81, s36 op_sel:[0,0,0,1]
	v_exp_f32_e32 v98, v98
	v_exp_f32_e32 v99, v99
	v_mfma_f32_32x32x64_f8f6f4 v[34:49], v[146:153], v[138:145], v[34:49]
	v_exp_f32_e32 v100, v100
	v_exp_f32_e32 v101, v101
	v_exp_f32_e32 v102, v102
	v_exp_f32_e32 v103, v103
	v_exp_f32_e32 v104, v104
	v_exp_f32_e32 v105, v105
	v_exp_f32_e32 v106, v106
	v_exp_f32_e32 v107, v107
	v_exp_f32_e32 v108, v108
	v_exp_f32_e32 v109, v109
	v_exp_f32_e32 v110, v110
	v_exp_f32_e32 v111, v111
	v_exp_f32_e32 v112, v112
	v_exp_f32_e32 v113, v113
	ds_read_b128 v[192:195], v219
	ds_read_b128 v[196:199], v219 offset:16
	v_pk_add_f32 v[66:67], v[232:233], v[98:99]
	v_pk_add_f32 v[68:69], v[230:231], v[100:101]
	v_pk_add_f32 v[66:67], v[102:103], v[66:67]
	v_pk_add_f32 v[68:69], v[104:105], v[68:69]
	v_pk_add_f32 v[66:67], v[106:107], v[66:67]
	v_pk_add_f32 v[68:69], v[108:109], v[68:69]
	v_pk_add_f32 v[140:141], v[110:111], v[66:67]
	v_pk_add_f32 v[138:139], v[112:113], v[68:69]
	v_mfma_f32_32x32x64_f8f6f4 v[18:33], v[146:153], v[130:137], v[18:33]
	v_exp_f32_e32 v82, v82
	v_exp_f32_e32 v83, v83
	v_exp_f32_e32 v84, v84
	v_exp_f32_e32 v85, v85
	v_exp_f32_e32 v86, v86
	v_exp_f32_e32 v87, v87
	v_exp_f32_e32 v88, v88
	v_exp_f32_e32 v89, v89
	v_exp_f32_e32 v90, v90
	v_exp_f32_e32 v91, v91
	v_exp_f32_e32 v92, v92
	v_exp_f32_e32 v93, v93
	v_exp_f32_e32 v94, v94
	v_exp_f32_e32 v95, v95
	v_exp_f32_e32 v96, v96
	v_exp_f32_e32 v97, v97
	v_pk_add_f32 v[66:67], v[190:191], v[82:83]
	v_pk_add_f32 v[68:69], v[188:189], v[84:85]
	v_pk_add_f32 v[66:67], v[86:87], v[66:67]
	v_pk_add_f32 v[68:69], v[88:89], v[68:69]
	v_pk_add_f32 v[130:131], v[90:91], v[66:67]
	v_pk_add_f32 v[132:133], v[92:93], v[68:69]
	s_waitcnt lgkmcnt(0)
; DI void attn_unit_d8(unsigned char* lds, const AttnArgs& a) {
;     ...
;     auto expsum = [&](f32x16& sc, f32x4& l) __attribute__((always_inline)) {
; #pragma unroll
;         for (int i = 0; i < 16; ++i) sc[i] = __builtin_amdgcn_exp2f(sc[i]);
; #pragma unroll
;         for (int i = 0; i < 4; ++i) l += (f32x4){sc[4 * i], sc[4 * i + 1], sc[4 * i + 2], sc[4 * i + 3]};
;     };
;     auto pack8 = [&](const f32x16& s0, const f32x16& s1) __attribute__((always_inline)) -> v8i { v8i p;
; #pragma unroll
;         for (int g = 0; g < 4; ++g) { p[g] = (int)pk4_fp8_div16(s0[4 * g], s0[4 * g + 1], s0[4 * g + 2], s0[4 * g + 3]); p[4 + g] = (int)pk4_fp8_div16(s1[4 * g], s1[4 * g + 1], s1[4 * g + 2], s1[4 * g + 3]); }
;         return p; };
;     auto pack4 = [&](const f32x16& sc, v8i& p, const int o) __attribute__((always_inline)) {
; #pragma unroll
;         for (int g = 0; g < 4; ++g) p[o + g] = (int)pk4_fp8_div16(sc[4 * g], sc[4 * g + 1], sc[4 * g + 2], sc[4 * g + 3]); };
;     auto qk = [&](const unsigned char* Kb, int hh, f32x16& sa, f32x16& sb) __attribute__((always_inline)) { const v8i kf = rd32(Kb + koff + hh * 32 * A8_PITCH);
;         sa = mfma8(kf, qfa, (f32x16){}); sb = mfma8(kf, qfb, (f32x16){}); };
;     gload(a.t0, kreg0, vreg0); gload(a.t0 + 1, kreg1, vreg1); lstore(0, kreg0, vreg0); lstore(1, kreg1, vreg1);
;     gload(a.t0 + 2, kreg0, vreg0); lstore(2, kreg0, vreg0);
;     __syncthreads();
;     asm volatile("" : "+v"(qfa), "+v"(qfb));
;     f32x16 s0a, s0b, s1a, s1b;
;     qk(lds, 0, s0a, s0b);
;     if (wid >= 4) __builtin_amdgcn_s_setprio(1);
;     int sb = 0;
;     const v8i zz8 = (v8i){0, 0, 0, 0, 0, 0, 0, 0};
;     v8i PaX = zz8, PbX = zz8, PaY = zz8, PbY = zz8, vX0 = zz8, vX1 = zz8, vY0 = zz8, vY1 = zz8;
;     auto tile = [&](const unsigned char* Kb, const unsigned char* Kn, v8i& Pa, v8i& Pb, v8i& v0, v8i& v1, const v8i& Qa, const v8i& Qb, const v8i& w0, const v8i& w1) __attribute__((always_inline)) {
;         qk(Kb, 1, s1a, s1b);
;         v0 = rd32(Kb + voff); v1 = rd32(Kb + voff + 32 * A8_PITCH);
;         o0[0] = mfma8(w0, Qa, o0[0]); o1[0] = mfma8(w0, Qb, o1[0]); o0[1] = mfma8(w1, Qa, o0[1]); o1[1] = mfma8(w1, Qb, o1[1]);
;         expsum(s0a, l0); expsum(s0b, l1); pack4(s0a, Pa, 0); pack4(s0b, Pb, 0);
;         qk(Kn, 0, s0a, s0b);
;         expsum(s1a, l0); expsum(s1b, l1); pack4(s1a, Pa, 4); pack4(s1b, Pb, 4);
	v_mfma_f32_32x32x64_f8f6f4 v[66:81], v[192:199], v[114:121], 0
	v_cvt_scalef32_pk_fp8_f32 v188, v98, v99, s36
	v_cvt_scalef32_pk_fp8_f32 v189, v102, v103, s36
	v_cvt_scalef32_pk_fp8_f32 v190, v106, v107, s36
	v_cvt_scalef32_pk_fp8_f32 v191, v110, v111, s36
	v_cvt_scalef32_pk_fp8_f32 v158, v82, v83, s36
	v_cvt_scalef32_pk_fp8_f32 v159, v86, v87, s36
	v_pk_add_f32 v[142:143], v[96:97], v[132:133]
	v_pk_add_f32 v[144:145], v[94:95], v[130:131]
	v_cvt_scalef32_pk_fp8_f32 v160, v90, v91, s36
	v_cvt_scalef32_pk_fp8_f32 v188, v100, v101, s36 op_sel:[0,0,0,1]
	v_cvt_scalef32_pk_fp8_f32 v189, v104, v105, s36 op_sel:[0,0,0,1]
	v_cvt_scalef32_pk_fp8_f32 v190, v108, v109, s36 op_sel:[0,0,0,1]
	v_cvt_scalef32_pk_fp8_f32 v191, v112, v113, s36 op_sel:[0,0,0,1]
	v_cvt_scalef32_pk_fp8_f32 v158, v84, v85, s36 op_sel:[0,0,0,1]
	v_cvt_scalef32_pk_fp8_f32 v159, v88, v89, s36 op_sel:[0,0,0,1]
	v_mfma_f32_32x32x64_f8f6f4 v[98:113], v[192:199], v[122:129], 0
	global_load_dwordx2 v[192:193], v[220:221], off
	global_load_dwordx2 v[194:195], v[222:223], off
	ds_read_b128 v[130:133], v219 offset:2560
	ds_read_b128 v[134:137], v219 offset:2576
	s_mulk_i32 s19, 0x2800
	v_exp_f32_e32 v146, v66
	v_exp_f32_e32 v147, v67
	v_exp_f32_e32 v148, v68
	v_exp_f32_e32 v149, v69
	s_add_i32 s19, s19, 0
	v_cvt_scalef32_pk_fp8_f32 v161, v94, v95, s36
	v_exp_f32_e32 v150, v70
	v_exp_f32_e32 v151, v71
	v_exp_f32_e32 v152, v72
	v_exp_f32_e32 v153, v73
	v_add_u32_e32 v224, s19, v216
	v_add_u32_e32 v225, s19, v217
	v_cvt_scalef32_pk_fp8_f32 v160, v92, v93, s36 op_sel:[0,0,0,1]
	v_cvt_scalef32_pk_fp8_f32 v161, v96, v97, s36 op_sel:[0,0,0,1]
	v_exp_f32_e32 v196, v74
	v_exp_f32_e32 v197, v75
	v_exp_f32_e32 v198, v76
	v_exp_f32_e32 v199, v77
	v_exp_f32_e32 v200, v78
	v_exp_f32_e32 v201, v79
	v_exp_f32_e32 v220, v80
	v_exp_f32_e32 v221, v81
	s_waitcnt lgkmcnt(0)
	v_mfma_f32_32x32x64_f8f6f4 v[82:97], v[130:137], v[114:121], 0
	v_add_f32_e64 v66, v140, v146
	v_add_f32_e64 v67, v141, v147
	v_add_f32_e64 v68, v138, v148
	v_add_f32_e64 v69, v139, v149
	v_add_f32_e64 v66, v150, v66
	v_add_f32_e64 v67, v151, v67
	v_add_f32_e64 v68, v152, v68
	v_add_f32_e64 v69, v153, v69
	v_add_f32_e64 v138, v196, v66
	v_add_f32_e64 v139, v197, v67
	v_add_f32_e64 v140, v198, v68
	v_add_f32_e64 v141, v199, v69
	v_exp_f32_e32 v98, v98
	v_exp_f32_e32 v99, v99
	v_exp_f32_e32 v100, v100
	v_exp_f32_e32 v101, v101
	v_exp_f32_e32 v102, v102
	v_exp_f32_e32 v103, v103
	v_exp_f32_e32 v104, v104
	v_exp_f32_e32 v105, v105
	v_exp_f32_e32 v106, v106
	v_exp_f32_e32 v107, v107
	v_exp_f32_e32 v108, v108
	v_exp_f32_e32 v109, v109
	v_exp_f32_e32 v110, v110
	v_exp_f32_e32 v111, v111
	v_exp_f32_e32 v112, v112
	v_exp_f32_e32 v113, v113
	v_mfma_f32_32x32x64_f8f6f4 v[66:81], v[130:137], v[122:129], 0
	v_add_f32_e64 v130, v144, v98
	v_add_f32_e64 v131, v145, v99
	v_add_f32_e64 v132, v142, v100
	v_add_f32_e64 v133, v143, v101
	v_add_f32_e64 v142, v102, v130
	v_add_f32_e64 v143, v103, v131
	v_add_f32_e64 v132, v104, v132
	v_add_f32_e64 v133, v105, v133
	v_add_f32_e64 v134, v220, v140
	v_add_f32_e64 v135, v221, v141
	v_add_f32_e64 v136, v200, v138
	v_add_f32_e64 v137, v201, v139
	v_pk_add_f32 v[142:143], v[106:107], v[142:143]
	v_pk_add_f32 v[132:133], v[108:109], v[132:133]
	v_cvt_scalef32_pk_fp8_f32 v138, v146, v147, s36
	v_cvt_scalef32_pk_fp8_f32 v139, v150, v151, s36
	v_cvt_scalef32_pk_fp8_f32 v140, v196, v197, s36
	v_cvt_scalef32_pk_fp8_f32 v141, v200, v201, s36
	v_cvt_scalef32_pk_fp8_f32 v130, v98, v99, s36
	v_cvt_scalef32_pk_fp8_f32 v131, v102, v103, s36
	v_pk_add_f32 v[146:147], v[112:113], v[132:133]
	v_pk_add_f32 v[150:151], v[110:111], v[142:143]
	v_mfma_f32_32x32x64_f8f6f4 v[50:65], v[170:177], v[184:191], v[50:65]
	v_exp_f32_e32 v82, v82
	v_exp_f32_e32 v83, v83
	v_exp_f32_e32 v84, v84
	v_exp_f32_e32 v85, v85
	v_add_u32_e32 v102, s17, v218
	v_exp_f32_e32 v86, v86
	v_exp_f32_e32 v87, v87
	v_exp_f32_e32 v88, v88
	v_exp_f32_e32 v89, v89
	v_cvt_scalef32_pk_fp8_f32 v130, v100, v101, s36 op_sel:[0,0,0,1]
	v_cvt_scalef32_pk_fp8_f32 v131, v104, v105, s36 op_sel:[0,0,0,1]
	v_exp_f32_e32 v90, v90
	v_exp_f32_e32 v91, v91
	v_exp_f32_e32 v92, v92
	v_exp_f32_e32 v93, v93
	ds_read_b128 v[98:101], v102
	ds_read_b128 v[102:105], v102 offset:16
	v_cvt_scalef32_pk_fp8_f32 v138, v148, v149, s36 op_sel:[0,0,0,1]
	v_cvt_scalef32_pk_fp8_f32 v139, v152, v153, s36 op_sel:[0,0,0,1]
	v_cvt_scalef32_pk_fp8_f32 v140, v198, v199, s36 op_sel:[0,0,0,1]
	v_cvt_scalef32_pk_fp8_f32 v141, v220, v221, s36 op_sel:[0,0,0,1]
	v_exp_f32_e32 v94, v94
	v_mfma_f32_32x32x64_f8f6f4 v[2:17], v[170:177], v[154:161], v[2:17]
	v_exp_f32_e32 v148, v96
	v_cvt_scalef32_pk_fp8_f32 v132, v106, v107, s36
	v_exp_f32_e32 v149, v97
	v_pk_add_f32 v[96:97], v[136:137], v[82:83]
; DI void attn_unit_a8(unsigned char* lds, const AttnArgs& a) {
;     ...
;     auto w_decode = [&](int j, const float*& src, unsigned char*& dst, int& ld, int& n0, int& k0, bool& gu) __attribute__((always_inline)) {
;         const int g = (j >> 2) * 512 + a.wl, e = g / 96, rr = g - e * 96; KParamsPtr kp = kparams();
;         if (rr < 64) { src = kp->w_gu + ((size_t)a.wli * NE + e) * (1024 * 2048); dst = kp->ws + WS_WGU + (size_t)a.wli * SZ_WGU + (size_t)e * 2048 * 1024; ld = 2048; n0 = (rr & 7) * 256; k0 = ((rr >> 3) * 4 + (j & 3)) * 32; gu = true; }
;         else { const int q = rr - 64; src = kp->w_dn + ((size_t)a.wli * NE + e) * (1024 * 1024); dst = kp->ws + WS_WDN + (size_t)a.wli * SZ_WDN + (size_t)e * 1024 * 1024; ld = 1024; n0 = (q & 3) * 256; k0 = ((q >> 2) * 4 + (j & 3)) * 32; gu = false; } };
;     auto w_issue = [&](int j) __attribute__((always_inline)) { const float* src; unsigned char* dst; int ld, n0, k0; bool gu; w_decode(j, src, dst, ld, n0, k0, gu);
;         const float* p = src + (size_t)(k0 + 4 * wid) * ld + n0 + wn4;
;         wq[0] = __builtin_nontemporal_load((const f32x4*)p); wq[1] = __builtin_nontemporal_load((const f32x4*)(p + ld));
;         wq[2] = __builtin_nontemporal_load((const f32x4*)(p + (size_t)2 * ld)); wq[3] = __builtin_nontemporal_load((const f32x4*)(p + (size_t)3 * ld)); };
;     auto w_cvt = [&]() __attribute__((always_inline)) { unsigned char* t8 = lds + AT_WT + wn4 * WPITCH + 4 * wid;
; #pragma unroll
;         for (int j = 0; j < 4; ++j) *(unsigned*)(t8 + j * WPITCH) = pk4_fp8_mul64(wq[0][j], wq[1][j], wq[2][j], wq[3][j]); };
; DI void attn_unit_d8(unsigned char* lds, const AttnArgs& a) {
;     ...
;     auto tile = [&](const unsigned char* Kb, const unsigned char* Kn, v8i& Pa, v8i& Pb, v8i& v0, v8i& v1, const v8i& Qa, const v8i& Qb, const v8i& w0, const v8i& w1) __attribute__((always_inline)) {
;         qk(Kb, 1, s1a, s1b);
;         v0 = rd32(Kb + voff); v1 = rd32(Kb + voff + 32 * A8_PITCH);
;         o0[0] = mfma8(w0, Qa, o0[0]); o1[0] = mfma8(w0, Qb, o1[0]); o0[1] = mfma8(w1, Qa, o0[1]); o1[1] = mfma8(w1, Qb, o1[1]);
;         expsum(s0a, l0); expsum(s0b, l1); pack4(s0a, Pa, 0); pack4(s0b, Pb, 0);
;         qk(Kn, 0, s0a, s0b);
;         expsum(s1a, l0); expsum(s1b, l1); pack4(s1a, Pa, 4); pack4(s1b, Pb, 4);
	v_pk_add_f32 v[106:107], v[134:135], v[84:85]
	v_exp_f32_e32 v66, v66
	v_exp_f32_e32 v67, v67
	v_exp_f32_e32 v68, v68
	v_exp_f32_e32 v69, v69
	v_exp_f32_e32 v95, v95
	v_cvt_scalef32_pk_fp8_f32 v133, v110, v111, s36
	v_pk_add_f32 v[106:107], v[88:89], v[106:107]
	v_pk_add_f32 v[96:97], v[86:87], v[96:97]
	v_exp_f32_e32 v70, v70
	v_exp_f32_e32 v71, v71
	v_exp_f32_e32 v72, v72
	v_exp_f32_e32 v73, v73
	v_cvt_scalef32_pk_fp8_f32 v132, v108, v109, s36 op_sel:[0,0,0,1]
	v_cvt_scalef32_pk_fp8_f32 v133, v112, v113, s36 op_sel:[0,0,0,1]
	v_pk_add_f32 v[96:97], v[90:91], v[96:97]
	v_pk_add_f32 v[106:107], v[92:93], v[106:107]
	v_exp_f32_e32 v74, v74
	v_mfma_f32_32x32x64_f8f6f4 v[34:49], v[162:169], v[184:191], v[34:49]
	v_exp_f32_e32 v75, v75
	v_exp_f32_e32 v76, v76
	v_exp_f32_e32 v77, v77
	v_exp_f32_e32 v78, v78
	v_exp_f32_e32 v79, v79
	v_exp_f32_e32 v80, v80
	v_exp_f32_e32 v81, v81
	v_cvt_scalef32_pk_fp8_f32 v142, v82, v83, s36
	v_cvt_scalef32_pk_fp8_f32 v143, v86, v87, s36
	v_cvt_scalef32_pk_fp8_f32 v144, v90, v91, s36
	v_cvt_scalef32_pk_fp8_f32 v142, v84, v85, s36 op_sel:[0,0,0,1]
	v_pk_add_f32 v[82:83], v[150:151], v[66:67]
	v_pk_add_f32 v[84:85], v[146:147], v[68:69]
	s_mulk_i32 s49, 0x2800
	v_pk_add_f32 v[184:185], v[148:149], v[106:107]
	v_pk_add_f32 v[186:187], v[94:95], v[96:97]
	v_cvt_scalef32_pk_fp8_f32 v145, v94, v95, s36
	v_cvt_scalef32_pk_fp8_f32 v143, v88, v89, s36 op_sel:[0,0,0,1]
	v_cvt_scalef32_pk_fp8_f32 v144, v92, v93, s36 op_sel:[0,0,0,1]
	v_mfma_f32_32x32x64_f8f6f4 v[18:33], v[162:169], v[154:161], v[18:33]
	v_add_f32_e64 v84, v72, v84
	v_add_f32_e64 v85, v73, v85
	v_add_f32_e64 v82, v70, v82
	v_add_f32_e64 v83, v71, v83
	s_add_i32 s6, s49, 0
	v_add_f32_e64 v82, v74, v82
	v_add_f32_e64 v83, v75, v83
	v_add_f32_e64 v84, v76, v84
	v_add_f32_e64 v85, v77, v85
	v_cvt_scalef32_pk_fp8_f32 v134, v66, v67, s36
	v_cvt_scalef32_pk_fp8_f32 v135, v70, v71, s36
	v_cvt_scalef32_pk_fp8_f32 v136, v74, v75, s36
	v_cvt_scalef32_pk_fp8_f32 v137, v78, v79, s36
	v_pk_add_f32 v[188:189], v[80:81], v[84:85]
	v_pk_add_f32 v[190:191], v[78:79], v[82:83]
	v_add_u32_e32 v106, s6, v216
	v_add_u32_e32 v107, s6, v217
	v_cvt_scalef32_pk_fp8_f32 v145, v148, v149, s36 op_sel:[0,0,0,1]
	v_cvt_scalef32_pk_fp8_f32 v134, v68, v69, s36 op_sel:[0,0,0,1]
	v_cvt_scalef32_pk_fp8_f32 v135, v72, v73, s36 op_sel:[0,0,0,1]
	v_cvt_scalef32_pk_fp8_f32 v136, v76, v77, s36 op_sel:[0,0,0,1]
	v_cvt_scalef32_pk_fp8_f32 v137, v80, v81, s36 op_sel:[0,0,0,1]
	s_waitcnt lgkmcnt(0)
	v_mfma_f32_32x32x64_f8f6f4 v[82:97], v[98:105], v[114:121], 0
	ds_read_b128 v[154:157], v219 offset:5120
	ds_read_b128 v[158:161], v219 offset:5136
	ds_read_b128 v[146:149], v219 offset:7680
	ds_read_b128 v[150:153], v219 offset:7696
	s_and_b32 s72, s61, 3
	s_cmp_eq_u32 s72, 0
	s_cbranch_scc0 .Lmy_rd0_nodec
	s_lshr_b32 s73, s61, 2
	s_lshl_b32 s73, s73, 9
	s_add_i32 s73, s73, s42
	s_mul_i32 s75, s73, 0xaaab
	s_lshr_b32 s75, s75, 22
	s_mul_i32 s76, s75, 0x60
	s_sub_i32 s76, s73, s76
	s_lshr_b32 s77, s76, 6
	s_lshl_b32 s78, s77, 6
	s_sub_i32 s76, s76, s78
	s_sub_i32 s78, 3, s77
	s_lshr_b32 s79, s76, s78
	s_lshl_b32 s79, s79, 2
	s_lshl_b32 s79, s79, 5
	s_lshl_b32 s81, s63, 2
	s_add_i32 s81, s81, s79
	s_sub_i32 s78, 13, s77
	s_lshl_b32 s81, s81, s78
	s_lshr_b32 s78, 7, s77
	s_and_b32 s78, s76, s78
	s_lshl_b32 s72, s78, 10
	s_add_i32 s81, s81, s72
	s_add_i32 s72, s75, 0
	s_sub_i32 s80, 23, s77
	s_lshl_b32 s72, s72, s80
	s_add_i32 s81, s81, s72
	s_cmp_eq_u32 s77, 0
	s_cselect_b64 s[84:85], s[66:67], s[68:69]
	s_add_u32 s84, s84, s81
	s_addc_u32 s85, s85, 0
	s_lshr_b32 s80, 0x2000, s77
	s_and_b32 s72, s78, 3
	s_lshl_b32 s72, s72, 19
	s_lshr_b32 s81, s78, 2
	s_lshl_b32 s81, s81, 17
	s_add_i32 s72, s72, s81
	s_lshl_b32 s81, s78, 18
	s_cmp_eq_u32 s77, 0
	s_cselect_b32 s72, s72, s81
	s_mul_i32 s81, s77, 0x10000000
	s_add_i32 s81, s81, 0x1094000
	s_add_i32 s72, s72, s79
	s_sub_i32 s73, 21, s77
	s_lshl_b32 s73, s75, s73
	s_add_i32 s72, s72, s73
	s_add_u32 s72, s72, s81
	s_or_b32 s79, s72, s77
.Lmy_rd0_nodec:
	s_cmpk_gt_i32 s42, 0x1ff
	s_cbranch_scc1 .Lmy_rd0_ldum
	s_add_i32 s72, s61, -1
	s_cmp_lt_u32 s72, 24
	s_cbranch_scc0 .Lmy_rd0_noc
	s_waitcnt vmcnt(4)
	v_cvt_scalef32_pk_fp8_f32 v236, v236, v240, s62
	v_cvt_scalef32_pk_fp8_f32 v237, v237, v241, s62
	v_cvt_scalef32_pk_fp8_f32 v238, v238, v242, s62
	v_cvt_scalef32_pk_fp8_f32 v239, v239, v243, s62
	v_cvt_scalef32_pk_fp8_f32 v236, v244, v248, s62 op_sel:[0,0,0,1]
	v_cvt_scalef32_pk_fp8_f32 v237, v245, v249, s62 op_sel:[0,0,0,1]
	v_cvt_scalef32_pk_fp8_f32 v238, v246, v250, s62 op_sel:[0,0,0,1]
	v_cvt_scalef32_pk_fp8_f32 v239, v247, v251, s62 op_sel:[0,0,0,1]
	ds_write_b32 v252, v236
	ds_write_b32 v252, v237 offset:36
	ds_write_b32 v252, v238 offset:72
	ds_write_b32 v252, v239 offset:108

; DI f32x16 mfma8(v8i a, v8i b, f32x16 c) { return __builtin_amdgcn_mfma_scale_f32_32x32x64_f8f6f4(a, b, c, 0, 0, 0, 0, 0, 0); }
; DI void attn_unit_a8(unsigned char* lds, const AttnArgs& a) {
;     ...
;     auto w_issue = [&](int j) __attribute__((always_inline)) { const float* src; unsigned char* dst; int ld, n0, k0; bool gu; w_decode(j, src, dst, ld, n0, k0, gu);
;         const float* p = src + (size_t)(k0 + 4 * wid) * ld + n0 + wn4;
;         wq[0] = __builtin_nontemporal_load((const f32x4*)p); wq[1] = __builtin_nontemporal_load((const f32x4*)(p + ld));
;         wq[2] = __builtin_nontemporal_load((const f32x4*)(p + (size_t)2 * ld)); wq[3] = __builtin_nontemporal_load((const f32x4*)(p + (size_t)3 * ld)); };
; DI void attn_unit_d8(unsigned char* lds, const AttnArgs& a) {
;     ...
;         lstore(s3, kreg0, vreg0); lstore(s4, kreg1, vreg1);
;         __syncthreads();
;         sb = s2;
;     }
;     o0[0] = mfma8(vY0, PaY, o0[0]); o1[0] = mfma8(vY0, PbY, o1[0]); o0[1] = mfma8(vY1, PaY, o0[1]); o1[1] = mfma8(vY1, PbY, o1[1]);
;     __builtin_amdgcn_s_setprio(0);
;     float lt0 = l0[0] + l0[1] + l0[2] + l0[3]; lt0 += __shfl_xor(lt0, 32);
;     float lt1 = l1[0] + l1[1] + l1[2] + l1[3]; lt1 += __shfl_xor(lt1, 32);
;     unsigned char* op = a.out8 + (size_t)(wid * 32 + r) * 1024 + 4 * h;
;     const float r0 = 16.0f / lt0, r1 = 16.0f * a.lam / lt1;
;     float ss = 0.f;
; #pragma unroll
;     for (int d = 0; d < 2; ++d)
; #pragma unroll
;         for (int i = 0; i < 16; ++i) { const float v = o0[d][i] * r0 - o1[d][i] * r1; o0[d][i] = v; ss += v * v; }
;     ss += __shfl_xor(ss, 32);
;     const float rinv = rsqrtf(ss * (1.0f / 64.0f) + EPS) * a.oscale * CAT_SCALE;
;     f32x4 ggv[2][4];
; #pragma unroll
;     for (int d = 0; d < 2; ++d)
; #pragma unroll
;         for (int g = 0; g < 4; ++g) ggv[d][g] = *(const f32x4*)(a.subg + 32 * d + 8 * g + 4 * h);
;     asm volatile("" : "+v"(ggv[0][0]), "+v"(ggv[1][3]));
.Lmy_rd0_lgo:
	global_load_dwordx4 v[236:239], v235, s[84:85] nt
	s_add_u32 s84, s84, s80
	s_addc_u32 s85, s85, 0
	global_load_dwordx4 v[240:243], v235, s[84:85] nt
	s_add_u32 s84, s84, s80
	s_addc_u32 s85, s85, 0
	global_load_dwordx4 v[244:247], v235, s[84:85] nt
	s_add_u32 s84, s84, s80
	s_addc_u32 s85, s85, 0
	global_load_dwordx4 v[248:251], v235, s[84:85] nt
	s_mov_b32 s65, s58
	s_mov_b32 s58, s79
	s_mul_i32 s72, s80, 29
	s_add_u32 s84, s84, s72
	s_addc_u32 s85, s85, 0
	s_add_i32 s79, s79, 32
	v_xor_b32_e32 v252, 0x4000, v252
	v_xor_b32_e32 v253, 0x4000, v253
	s_add_i32 s61, s61, 1
	s_add_i32 s18, s46, 2
	s_cmpk_lt_u32 s46, 0x42
	s_mov_b32 s46, s18
	s_waitcnt vmcnt(6)
	ds_write_b64 v224, v[192:193]
	v_mfma_f32_32x32x64_f8f6f4 v[66:81], v[98:105], v[122:129], 0
	v_add_u32_e32 v98, 0x1400, v225
	v_add_u32_e32 v99, 0x1400, v107
	ds_write2_b32 v98, v202, v203 offset1:8
	s_waitcnt vmcnt(5)
	ds_write_b64 v106, v[194:195]
	ds_write2_b32 v99, v204, v205 offset1:8
	s_waitcnt lgkmcnt(0)
	s_barrier
	s_cbranch_scc1 .LBB0_663
	s_lshl_b64 s[14:15], s[14:15], 10
	s_add_u32 s6, s8, s14
	s_addc_u32 s15, s9, s15
	s_add_u32 s14, s6, s43
	v_mfma_f32_32x32x64_f8f6f4 v[50:65], v[154:161], v[138:145], v[50:65]
	s_addc_u32 s15, s15, 0
	v_mfma_f32_32x32x64_f8f6f4 v[2:17], v[154:161], v[130:137], v[2:17]
	v_mfma_f32_32x32x64_f8f6f4 v[34:49], v[146:153], v[138:145], v[34:49]
	v_mfma_f32_32x32x64_f8f6f4 v[18:33], v[146:153], v[130:137], v[18:33]
	s_setprio 0
	v_add_f32_e32 v66, v186, v187
	v_add_f32_e32 v66, v184, v66
	v_add_f32_e32 v66, v185, v66
	ds_bpermute_b32 v67, v1, v66
	v_add_f32_e32 v68, v190, v191
	v_add_f32_e32 v68, v188, v68
	v_add_f32_e32 v68, v189, v68
	ds_bpermute_b32 v69, v1, v68
	s_waitcnt lgkmcnt(1)
	v_add_f32_e32 v66, v66, v67
	v_div_scale_f32 v67, s[16:17], v66, v66, s36
	v_rcp_f32_e32 v70, v67
	s_waitcnt lgkmcnt(0)
	v_add_f32_e32 v68, v68, v69
	v_lshlrev_b32_e32 v178, 2, v214
	s_add_i32 s42, s42, s64
	v_fma_f32 v69, -v67, v70, 1.0
	v_fmac_f32_e32 v70, v69, v70
	v_div_scale_f32 v69, vcc, s36, v66, s36
	v_mul_f32_e32 v71, v69, v70
	v_fma_f32 v72, -v67, v71, v69
	v_fmac_f32_e32 v71, v72, v70
	v_fma_f32 v67, -v67, v71, v69
	v_div_scale_f32 v69, s[16:17], v68, v68, v211
	v_rcp_f32_e32 v72, v69
	v_div_fmas_f32 v67, v67, v70, v71
	v_div_fixup_f32 v66, v67, v66, s36
	s_cmpk_gt_i32 s42, 0x21f
	v_fma_f32 v67, -v69, v72, 1.0
	v_fmac_f32_e32 v72, v67, v72
	v_div_scale_f32 v67, vcc, v211, v68, v211
	v_mul_f32_e32 v70, v67, v72
	v_fma_f32 v71, -v69, v70, v67
	v_fmac_f32_e32 v70, v71, v72
	v_fma_f32 v67, -v69, v70, v67
	v_div_fmas_f32 v67, v67, v72, v70
	v_div_fixup_f32 v68, v67, v68, v211
	v_mul_f32_e32 v2, v2, v68
	v_fma_f32 v50, v50, v66, -v2
	v_mul_f32_e32 v2, v3, v68
	v_fma_f32 v51, v51, v66, -v2
	v_mul_f32_e32 v67, v51, v51
	v_mul_f32_e32 v2, v4, v68
	v_fmac_f32_e32 v67, v50, v50
	v_fma_f32 v52, v52, v66, -v2
	v_mul_f32_e32 v2, v5, v68
	v_fmac_f32_e32 v67, v52, v52
	v_fma_f32 v53, v53, v66, -v2
	v_mul_f32_e32 v2, v6, v68
	v_fmac_f32_e32 v67, v53, v53
	v_fma_f32 v54, v54, v66, -v2
	v_mul_f32_e32 v2, v7, v68
	v_fmac_f32_e32 v67, v54, v54
	v_fma_f32 v55, v55, v66, -v2
	v_mul_f32_e32 v2, v8, v68
	v_fmac_f32_e32 v67, v55, v55
	v_fma_f32 v56, v56, v66, -v2
	v_mul_f32_e32 v2, v9, v68
	v_fmac_f32_e32 v67, v56, v56
	v_fma_f32 v57, v57, v66, -v2
	v_mul_f32_e32 v2, v10, v68
	v_fmac_f32_e32 v67, v57, v57
	v_fma_f32 v58, v58, v66, -v2
	v_mul_f32_e32 v2, v11, v68
	v_fmac_f32_e32 v67, v58, v58
	v_fma_f32 v59, v59, v66, -v2
	v_mul_f32_e32 v2, v12, v68
	v_fmac_f32_e32 v67, v59, v59
	v_fma_f32 v60, v60, v66, -v2
	v_mul_f32_e32 v2, v13, v68
	v_fmac_f32_e32 v67, v60, v60
	v_fma_f32 v61, v61, v66, -v2
	v_mul_f32_e32 v14, v14, v68
	v_fmac_f32_e32 v67, v61, v61
	v_fma_f32 v62, v62, v66, -v14
	v_mul_f32_e32 v14, v15, v68
	v_fmac_f32_e32 v67, v62, v62
	v_fma_f32 v63, v63, v66, -v14
	v_mul_f32_e32 v14, v16, v68
	v_lshlrev_b32_e32 v69, 4, v214
	v_fmac_f32_e32 v67, v63, v63
	v_fma_f32 v64, v64, v66, -v14
	v_mul_f32_e32 v14, v17, v68
	global_load_dwordx4 v[2:5], v69, s[10:11] offset:224
	global_load_dwordx4 v[6:9], v69, s[10:11] offset:32
	global_load_dwordx4 v[10:13], v69, s[10:11]
	v_fmac_f32_e32 v67, v64, v64
	v_fma_f32 v65, v65, v66, -v14
	v_mul_f32_e32 v14, v18, v68
	v_fmac_f32_e32 v67, v65, v65
	v_fma_f32 v70, v34, v66, -v14
	v_mul_f32_e32 v14, v19, v68
	v_fmac_f32_e32 v67, v70, v70
	v_fma_f32 v71, v35, v66, -v14
	v_mul_f32_e32 v14, v20, v68
	v_fmac_f32_e32 v67, v71, v71
	v_fma_f32 v72, v36, v66, -v14
	v_mul_f32_e32 v14, v21, v68
	v_fmac_f32_e32 v67, v72, v72
	v_fma_f32 v73, v37, v66, -v14
	v_mul_f32_e32 v14, v22, v68
	v_fmac_f32_e32 v67, v73, v73
	v_fma_f32 v74, v38, v66, -v14
	v_mul_f32_e32 v14, v23, v68
	v_fmac_f32_e32 v67, v74, v74
	v_fma_f32 v75, v39, v66, -v14
	v_fmac_f32_e32 v67, v75, v75
	v_pk_mul_f32 v[14:15], v[24:25], v[68:69] op_sel_hi:[1,0]
	v_pk_mul_f32 v[22:23], v[32:33], v[68:69] op_sel_hi:[1,0]
	v_pk_fma_f32 v[34:35], v[40:41], v[66:67], v[14:15] op_sel_hi:[1,0,1] neg_lo:[0,0,1] neg_hi:[0,0,1]
	s_nop 0
	v_pk_mul_f32 v[14:15], v[34:35], v[34:35]
	s_nop 0
	v_add_f32_e32 v14, v14, v67
	v_add_f32_e32 v20, v15, v14
	v_pk_mul_f32 v[14:15], v[26:27], v[68:69] op_sel_hi:[1,0]
	s_nop 0
	v_pk_fma_f32 v[36:37], v[42:43], v[66:67], v[14:15] op_sel_hi:[1,0,1] neg_lo:[0,0,1] neg_hi:[0,0,1]
	global_load_dwordx4 v[14:17], v69, s[10:11] offset:64
	v_pk_mul_f32 v[18:19], v[36:37], v[36:37]
	v_pk_fma_f32 v[42:43], v[48:49], v[66:67], v[22:23] op_sel_hi:[1,0,1] neg_lo:[0,0,1] neg_hi:[0,0,1]
	v_add_f32_e32 v18, v18, v20
	v_add_f32_e32 v20, v19, v18
	v_pk_mul_f32 v[18:19], v[28:29], v[68:69] op_sel_hi:[1,0]
	v_pk_mul_f32 v[22:23], v[42:43], v[42:43]
	v_pk_fma_f32 v[38:39], v[44:45], v[66:67], v[18:19] op_sel_hi:[1,0,1] neg_lo:[0,0,1] neg_hi:[0,0,1]
	s_nop 0
	v_pk_mul_f32 v[18:19], v[38:39], v[38:39]
	s_nop 0
	v_add_f32_e32 v18, v18, v20
	v_add_f32_e32 v20, v19, v18
	v_pk_mul_f32 v[18:19], v[30:31], v[68:69] op_sel_hi:[1,0]
	s_nop 0
	v_pk_fma_f32 v[40:41], v[46:47], v[66:67], v[18:19] op_sel_hi:[1,0,1] neg_lo:[0,0,1] neg_hi:[0,0,1]
	s_nop 0
	v_pk_mul_f32 v[18:19], v[40:41], v[40:41]
	s_nop 0
	v_add_f32_e32 v18, v18, v20
	v_add_f32_e32 v24, v19, v18
	v_add_f32_e32 v22, v22, v24
	v_add_f32_e32 v26, v23, v22
	ds_bpermute_b32 v27, v1, v26
	global_load_dwordx4 v[18:21], v69, s[10:11] offset:96
	global_load_dwordx4 v[22:25], v69, s[10:11] offset:192
	s_waitcnt lgkmcnt(0)
; DI unsigned pk4_fp8(float a, float b, float c, float d) { int r = 0; r = __builtin_amdgcn_cvt_pk_fp8_f32(a, b, r, false); r = __builtin_amdgcn_cvt_pk_fp8_f32(c, d, r, true); return (unsigned)r; }
; DI float clamp448(float x) { return __builtin_amdgcn_fmed3f(x, -448.0f, 448.0f); }
; DI void attn_unit_d8(unsigned char* lds, const AttnArgs& a) {
;     ...
;     ss += __shfl_xor(ss, 32);
;     const float rinv = rsqrtf(ss * (1.0f / 64.0f) + EPS) * a.oscale * CAT_SCALE;
;     f32x4 ggv[2][4];
; #pragma unroll
;     for (int d = 0; d < 2; ++d)
; #pragma unroll
;         for (int g = 0; g < 4; ++g) ggv[d][g] = *(const f32x4*)(a.subg + 32 * d + 8 * g + 4 * h);
;     asm volatile("" : "+v"(ggv[0][0]), "+v"(ggv[1][3]));
; #pragma unroll
;     for (int d = 0; d < 2; ++d)
; #pragma unroll
;         for (int g = 0; g < 4; ++g) { const f32x4 gg = ggv[d][g];
;             *(unsigned*)(op + 32 * d + 8 * g) = pk4_fp8(clamp448(o0[d][4 * g] * rinv * gg[0]), clamp448(o0[d][4 * g + 1] * rinv * gg[1]), clamp448(o0[d][4 * g + 2] * rinv * gg[2]), clamp448(o0[d][4 * g + 3] * rinv * gg[3])); }
	v_add_f32_e32 v26, v26, v27
	v_fmamk_f32 v26, v26, 0x3c800000, v212
	v_mul_f32_e32 v27, 0x4b800000, v26
	v_cmp_gt_f32_e32 vcc, s39, v26
	s_nop 1
	v_cndmask_b32_e32 v30, v26, v27, vcc
	global_load_dwordx4 v[26:29], v69, s[10:11] offset:128
	v_rsq_f32_e32 v32, v30
	v_lshlrev_b64 v[30:31], 10, v[180:181]
	v_lshl_add_u64 v[44:45], s[14:15], 0, v[30:31]
	v_lshl_add_u64 v[44:45], v[44:45], 0, v[178:179]
	v_mul_f32_e32 v30, 0x45800000, v32
	v_cndmask_b32_e32 v30, v32, v30, vcc
	v_mul_f32_e32 v48, 0x3f4ccccd, v30
	global_load_dwordx4 v[30:33], v69, s[10:11] offset:160
	v_mul_f32_e32 v48, 0x41800000, v48
	s_waitcnt vmcnt(5)
	v_mul_f32_e32 v49, v50, v48
	v_mul_f32_e32 v10, v10, v49
	v_mul_f32_e32 v49, v51, v48
	v_mul_f32_e32 v11, v11, v49
	v_mul_f32_e32 v49, v52, v48
	v_med3_f32 v10, v10, s40, v213
	v_med3_f32 v11, v11, s40, v213
	v_mul_f32_e32 v12, v12, v49
	s_nop 0
	v_cvt_pk_fp8_f32 v49, v10, v11
	v_mul_f32_e32 v10, v53, v48
	v_mul_f32_e32 v10, v13, v10
	v_med3_f32 v12, v12, s40, v213
	v_med3_f32 v10, v10, s40, v213
	v_cvt_pk_fp8_f32 v49, v12, v10 op_sel:[0,0,1]
	v_mul_f32_e32 v10, v54, v48
	v_mul_f32_e32 v6, v6, v10
	v_mul_f32_e32 v10, v55, v48
	v_mul_f32_e32 v7, v7, v10
	v_mul_f32_e32 v10, v56, v48
	v_med3_f32 v6, v6, s40, v213
	v_med3_f32 v7, v7, s40, v213
	v_mul_f32_e32 v8, v8, v10
	s_nop 0
	v_cvt_pk_fp8_f32 v10, v6, v7
	v_mul_f32_e32 v6, v57, v48
	v_mul_f32_e32 v6, v9, v6
	v_med3_f32 v8, v8, s40, v213
	v_med3_f32 v6, v6, s40, v213
	v_cvt_pk_fp8_f32 v10, v8, v6 op_sel:[0,0,1]
	v_add_co_u32_e32 v6, vcc, s41, v44
	v_lshl_add_u64 v[46:47], v[44:45], 0, s[12:13]
	s_nop 0
	v_addc_co_u32_e32 v7, vcc, 0, v45, vcc
	global_store_dword v[6:7], v49, off offset:768
	global_store_dword v[46:47], v10, off offset:8
	v_mul_f32_e32 v6, v58, v48
	v_mul_f32_e32 v7, v59, v48
	s_waitcnt vmcnt(6)
	v_mul_f32_e32 v6, v14, v6
	v_mul_f32_e32 v7, v15, v7
	v_med3_f32 v6, v6, s40, v213
	v_med3_f32 v7, v7, s40, v213
	s_nop 0
	v_cvt_pk_fp8_f32 v9, v6, v7
	v_mul_f32_e32 v8, v60, v48
	v_mul_f32_e32 v6, v61, v48
	v_mul_f32_e32 v8, v16, v8
	v_mul_f32_e32 v6, v17, v6
	v_med3_f32 v8, v8, s40, v213
	v_med3_f32 v6, v6, s40, v213
	v_cvt_pk_fp8_f32 v9, v8, v6 op_sel:[0,0,1]
	v_mul_f32_e32 v6, v62, v48
	v_mul_f32_e32 v7, v63, v48
	s_nop 0
	v_mul_f32_e32 v8, v64, v48
	s_nop 0
	s_waitcnt vmcnt(5)
	v_mul_f32_e32 v6, v18, v6
	v_mul_f32_e32 v7, v19, v7
	v_med3_f32 v6, v6, s40, v213
	v_med3_f32 v7, v7, s40, v213
	v_cvt_pk_fp8_f32 v10, v6, v7
	v_mul_f32_e32 v6, v65, v48
	v_mul_f32_e32 v8, v20, v8
	v_mul_f32_e32 v6, v21, v6
	v_med3_f32 v8, v8, s40, v213
	v_med3_f32 v6, v6, s40, v213
	v_cvt_pk_fp8_f32 v10, v8, v6 op_sel:[0,0,1]
	v_mul_f32_e32 v6, v70, v48
	v_mul_f32_e32 v7, v71, v48
	s_waitcnt vmcnt(3)
	v_mul_f32_e32 v6, v26, v6
	v_mul_f32_e32 v7, v27, v7
	v_med3_f32 v6, v6, s40, v213
	v_med3_f32 v7, v7, s40, v213
	v_cvt_pk_fp8_f32 v11, v6, v7
	v_mul_f32_e32 v8, v72, v48
	v_mul_f32_e32 v6, v73, v48
	v_mul_f32_e32 v8, v28, v8
	v_mul_f32_e32 v6, v29, v6
	v_med3_f32 v8, v8, s40, v213
	v_med3_f32 v6, v6, s40, v213
	v_cvt_pk_fp8_f32 v11, v8, v6 op_sel:[0,0,1]
	v_mul_f32_e32 v6, v74, v48
	v_mul_f32_e32 v7, v75, v48
	s_waitcnt vmcnt(2)
	v_mul_f32_e32 v6, v30, v6
	v_mul_f32_e32 v7, v31, v7
	v_med3_f32 v6, v6, s40, v213
	v_med3_f32 v7, v7, s40, v213
	s_nop 0
	v_cvt_pk_fp8_f32 v12, v6, v7
	v_mul_f32_e32 v8, v34, v48
	v_mul_f32_e32 v6, v35, v48
	v_mul_f32_e32 v8, v32, v8
	v_mul_f32_e32 v6, v33, v6
	v_med3_f32 v8, v8, s40, v213
	v_med3_f32 v6, v6, s40, v213
	v_cvt_pk_fp8_f32 v12, v8, v6 op_sel:[0,0,1]
	v_mul_f32_e32 v6, v36, v48
	v_mul_f32_e32 v7, v37, v48
	v_mul_f32_e32 v6, v22, v6
	v_mul_f32_e32 v7, v23, v7
	global_store_dword v[46:47], v9, off offset:16
	global_store_dword v[46:47], v10, off offset:24
	global_store_dword v[46:47], v11, off offset:32
	global_store_dword v[46:47], v12, off offset:40
	v_med3_f32 v6, v6, s40, v213
	v_med3_f32 v7, v7, s40, v213
	s_nop 0
	v_cvt_pk_fp8_f32 v9, v6, v7
	v_mul_f32_e32 v8, v38, v48
	v_mul_f32_e32 v6, v39, v48
	v_mul_f32_e32 v8, v24, v8
	v_mul_f32_e32 v6, v25, v6
	v_med3_f32 v8, v8, s40, v213
	v_med3_f32 v6, v6, s40, v213
	v_cvt_pk_fp8_f32 v9, v8, v6 op_sel:[0,0,1]
	v_mul_f32_e32 v6, v40, v48
	v_mul_f32_e32 v2, v2, v6
	v_mul_f32_e32 v6, v41, v48
	v_mul_f32_e32 v3, v3, v6
	v_mul_f32_e32 v6, v42, v48
	v_med3_f32 v2, v2, s40, v213
	v_med3_f32 v3, v3, s40, v213
	v_mul_f32_e32 v4, v4, v6
	s_nop 0
	v_cvt_pk_fp8_f32 v6, v2, v3
	v_mul_f32_e32 v2, v43, v48
	v_mul_f32_e32 v2, v5, v2
	v_med3_f32 v4, v4, s40, v213
	v_med3_f32 v2, v2, s40, v213
	v_cvt_pk_fp8_f32 v6, v4, v2 op_sel:[0,0,1]
	global_store_dword v[46:47], v9, off offset:48
	global_store_dword v[46:47], v6, off offset:56
	s_cbranch_scc0 .LBB0_656

; DI f32x16 mfma8(v8i a, v8i b, f32x16 c) { return __builtin_amdgcn_mfma_scale_f32_32x32x64_f8f6f4(a, b, c, 0, 0, 0, 0, 0, 0); }
; DI void attn_unit_d8(unsigned char* lds, const AttnArgs& a) {
;     ...
;     auto tile = [&](const unsigned char* Kb, const unsigned char* Kn, v8i& Pa, v8i& Pb, v8i& v0, v8i& v1, const v8i& Qa, const v8i& Qb, const v8i& w0, const v8i& w1) __attribute__((always_inline)) {
;         qk(Kb, 1, s1a, s1b);
;         v0 = rd32(Kb + voff); v1 = rd32(Kb + voff + 32 * A8_PITCH);
;         o0[0] = mfma8(w0, Qa, o0[0]); o1[0] = mfma8(w0, Qb, o1[0]); o0[1] = mfma8(w1, Qa, o0[1]); o1[1] = mfma8(w1, Qb, o1[1]);
;         expsum(s0a, l0); expsum(s0b, l1); pack4(s0a, Pa, 0); pack4(s0b, Pb, 0);
;         qk(Kn, 0, s0a, s0b);
;         expsum(s1a, l0); expsum(s1b, l1); pack4(s1a, Pa, 4); pack4(s1b, Pb, 4);
; #pragma unroll
;         for (int i = 0; i < 8; ++i) { __builtin_amdgcn_sched_group_barrier(0x008, 1, 0); __builtin_amdgcn_sched_group_barrier(0x402, 22, 0); }
;     };
;     for (int t = a.t0; t < a.t1; t += 2) {
;         const int s1 = sb + 1 >= 5 ? sb - 4 : sb + 1, s2 = sb + 2 >= 5 ? sb - 3 : sb + 2, s3 = sb + 3 >= 5 ? sb - 2 : sb + 3, s4 = sb + 4 >= 5 ? sb - 1 : sb + 4;
;         { const int ta = t + 3, tb = t + 4; gload(ta < a.t1 ? ta : a.t1 - 1, kreg0, vreg0); gload(tb < a.t1 ? tb : a.t1 - 1, kreg1, vreg1); }
;         tile(lds + sb * D8_SLOT, lds + s1 * D8_SLOT, PaX, PbX, vX0, vX1, PaY, PbY, vY0, vY1);
.LBB0_1888:
	s_add_i32 s22, s22, 2
	s_mul_i32 s8, s23, 0x2800
	s_cmp_gt_i32 s23, 3
	v_mfma_f32_32x32x64_f8f6f4 v[50:65], v[154:161], v[138:145], v[50:65]
	v_exp_f32_e32 v194, v90
	v_add_u32_e32 v90, s8, v219
	s_cselect_b32 s8, -4, 1
	s_add_i32 s51, s8, s23
	s_cmp_gt_i32 s23, 2
	s_cselect_b32 s8, -3, 2
	s_add_i32 s8, s8, s23
	s_cmp_gt_i32 s23, 1
	s_cselect_b32 s52, -2, 3
	s_add_i32 s52, s52, s23
	s_cmp_gt_i32 s23, 0
	s_cselect_b32 s53, -1, 4
	s_min_u32 s56, s22, 64
	s_add_i32 s53, s53, s23
	s_cmp_lt_u32 s22, 61
	s_mul_i32 s50, s8, 0x2800
	s_mov_b32 s23, s8
	s_cselect_b64 s[54:55], -1, 0
	s_lshl_b32 s8, s56, 6
	s_add_i32 s56, s8, 0xc0
	s_add_i32 s57, s8, 0xfffff0c0
	s_and_b64 s[54:55], s[54:55], exec
	v_lshl_add_u64 v[98:99], v[184:185], 0, s[8:9]
	s_cselect_b32 s8, s56, s57
	s_cselect_b32 s55, s19, s21
	s_cselect_b32 s54, s18, s20
	s_min_u32 s58, s22, 63
	v_exp_f32_e32 v200, v82
	v_exp_f32_e32 v201, v83
	v_exp_f32_e32 v198, v84
	v_exp_f32_e32 v199, v85
	v_exp_f32_e32 v202, v86
	v_exp_f32_e32 v203, v87
	v_exp_f32_e32 v196, v88
	v_exp_f32_e32 v197, v89
	ds_read_b128 v[82:85], v90 offset:2560
	ds_read_b128 v[86:89], v90 offset:2576
	global_load_dwordx2 v[204:205], v[98:99], off offset:192
	v_add_u32_e32 v98, s8, v182
	s_cmp_lt_u32 s22, 60
	v_ashrrev_i32_e32 v99, 31, v98
	s_cselect_b64 s[56:57], -1, 0
	s_lshl_b32 s8, s58, 6
	v_lshlrev_b64 v[98:99], 8, v[98:99]
	s_add_i32 s58, s8, 0x100
	s_add_i32 s59, s8, 0xfffff100
	v_lshl_add_u64 v[98:99], s[54:55], 0, v[98:99]
	s_and_b64 s[54:55], s[56:57], exec
	v_lshl_add_u64 v[100:101], v[184:185], 0, s[8:9]
	s_cselect_b32 s8, s58, s59
	v_lshl_add_u64 v[220:221], v[98:99], 0, v[178:179]
	v_add_u32_e32 v98, s8, v182
	v_ashrrev_i32_e32 v99, 31, v98
	s_cselect_b32 s55, s19, s21
	s_cselect_b32 s54, s18, s20
	v_lshlrev_b64 v[98:99], 8, v[98:99]
	v_lshl_add_u64 v[98:99], s[54:55], 0, v[98:99]
	global_load_dwordx2 v[206:207], v[100:101], off offset:256
	v_lshl_add_u64 v[222:223], v[98:99], 0, v[178:179]
	s_waitcnt lgkmcnt(0)
	v_mfma_f32_32x32x64_f8f6f4 v[98:113], v[82:89], v[114:121], 0
	v_exp_f32_e32 v195, v91
	v_exp_f32_e32 v224, v92
	v_exp_f32_e32 v225, v93
	v_exp_f32_e32 v226, v94
	v_exp_f32_e32 v227, v95
	v_exp_f32_e32 v228, v96
	v_exp_f32_e32 v229, v97
	ds_read_b128 v[170:173], v90 offset:5120
	ds_read_b128 v[174:177], v90 offset:5136
	ds_read_b128 v[162:165], v90 offset:7680
	ds_read_b128 v[166:169], v90 offset:7696
	v_pk_add_f32 v[90:91], v[188:189], v[200:201]
	v_pk_add_f32 v[92:93], v[186:187], v[198:199]
	v_pk_add_f32 v[90:91], v[202:203], v[90:91]
	v_pk_add_f32 v[92:93], v[196:197], v[92:93]
	v_pk_add_f32 v[90:91], v[194:195], v[90:91]
	v_pk_add_f32 v[92:93], v[224:225], v[92:93]
	v_exp_f32_e32 v66, v66
	v_exp_f32_e32 v67, v67
	v_exp_f32_e32 v68, v68
	v_exp_f32_e32 v69, v69
	v_exp_f32_e32 v70, v70
	v_exp_f32_e32 v71, v71
	v_exp_f32_e32 v72, v72
	v_pk_add_f32 v[230:231], v[228:229], v[92:93]
	v_pk_add_f32 v[232:233], v[226:227], v[90:91]
	v_mfma_f32_32x32x64_f8f6f4 v[82:97], v[82:89], v[122:129], 0
	v_exp_f32_e32 v73, v73
	v_exp_f32_e32 v74, v74
	v_exp_f32_e32 v75, v75
	v_exp_f32_e32 v76, v76
	v_exp_f32_e32 v77, v77
	v_exp_f32_e32 v78, v78
	v_exp_f32_e32 v79, v79
	v_exp_f32_e32 v80, v80
	v_exp_f32_e32 v81, v81
	v_pk_add_f32 v[188:189], v[192:193], v[66:67]
	v_pk_add_f32 v[190:191], v[190:191], v[68:69]
	v_pk_add_f32 v[188:189], v[70:71], v[188:189]
	v_pk_add_f32 v[190:191], v[72:73], v[190:191]
	v_cvt_scalef32_pk_fp8_f32 v186, v200, v201, s36
	v_pk_add_f32 v[188:189], v[74:75], v[188:189]
	v_pk_add_f32 v[190:191], v[76:77], v[190:191]
	v_cvt_scalef32_pk_fp8_f32 v187, v202, v203, s36
	v_cvt_scalef32_pk_fp8_f32 v186, v198, v199, s36 op_sel:[0,0,0,1]
	v_pk_add_f32 v[192:193], v[78:79], v[188:189]
	v_pk_add_f32 v[190:191], v[80:81], v[190:191]
	v_mfma_f32_32x32x64_f8f6f4 v[2:17], v[154:161], v[130:137], v[2:17]
	s_mulk_i32 s51, 0x2800
	v_cvt_scalef32_pk_fp8_f32 v188, v194, v195, s36
	v_cvt_scalef32_pk_fp8_f32 v189, v226, v227, s36
	v_cvt_scalef32_pk_fp8_f32 v154, v66, v67, s36
	v_cvt_scalef32_pk_fp8_f32 v155, v70, v71, s36
	v_cvt_scalef32_pk_fp8_f32 v156, v74, v75, s36
	v_cvt_scalef32_pk_fp8_f32 v157, v78, v79, s36
	v_cvt_scalef32_pk_fp8_f32 v187, v196, v197, s36 op_sel:[0,0,0,1]
	v_add_u32_e32 v234, s51, v219
	v_cvt_scalef32_pk_fp8_f32 v188, v224, v225, s36 op_sel:[0,0,0,1]
	v_cvt_scalef32_pk_fp8_f32 v189, v228, v229, s36 op_sel:[0,0,0,1]
	v_cvt_scalef32_pk_fp8_f32 v154, v68, v69, s36 op_sel:[0,0,0,1]
	v_cvt_scalef32_pk_fp8_f32 v155, v72, v73, s36 op_sel:[0,0,0,1]
	v_cvt_scalef32_pk_fp8_f32 v156, v76, v77, s36 op_sel:[0,0,0,1]
	v_cvt_scalef32_pk_fp8_f32 v157, v80, v81, s36 op_sel:[0,0,0,1]
	v_exp_f32_e32 v98, v98
	v_exp_f32_e32 v99, v99
	v_mfma_f32_32x32x64_f8f6f4 v[34:49], v[146:153], v[138:145], v[34:49]
	v_exp_f32_e32 v100, v100
	v_exp_f32_e32 v101, v101
	v_exp_f32_e32 v102, v102
	v_exp_f32_e32 v103, v103
	v_exp_f32_e32 v104, v104
	v_exp_f32_e32 v105, v105
	v_exp_f32_e32 v106, v106
	v_exp_f32_e32 v107, v107
	v_exp_f32_e32 v108, v108
	v_exp_f32_e32 v109, v109
	v_exp_f32_e32 v110, v110
	v_exp_f32_e32 v111, v111
	v_exp_f32_e32 v112, v112
	v_exp_f32_e32 v113, v113
	ds_read_b128 v[194:197], v234
	ds_read_b128 v[198:201], v234 offset:16
	v_pk_add_f32 v[66:67], v[232:233], v[98:99]
	v_pk_add_f32 v[68:69], v[230:231], v[100:101]
	v_pk_add_f32 v[66:67], v[102:103], v[66:67]
	v_pk_add_f32 v[68:69], v[104:105], v[68:69]
	v_pk_add_f32 v[66:67], v[106:107], v[66:67]
	v_pk_add_f32 v[68:69], v[108:109], v[68:69]
	v_pk_add_f32 v[140:141], v[110:111], v[66:67]
	v_pk_add_f32 v[138:139], v[112:113], v[68:69]
	v_mfma_f32_32x32x64_f8f6f4 v[18:33], v[146:153], v[130:137], v[18:33]
	v_exp_f32_e32 v82, v82
	v_exp_f32_e32 v83, v83
	v_exp_f32_e32 v84, v84
	v_exp_f32_e32 v85, v85
	v_exp_f32_e32 v86, v86
	v_exp_f32_e32 v87, v87
	v_exp_f32_e32 v88, v88
	v_exp_f32_e32 v89, v89
	v_exp_f32_e32 v90, v90
	v_exp_f32_e32 v91, v91
	v_exp_f32_e32 v92, v92
	v_exp_f32_e32 v93, v93
	v_exp_f32_e32 v94, v94
	v_exp_f32_e32 v95, v95
	v_exp_f32_e32 v96, v96
	v_exp_f32_e32 v97, v97
	v_pk_add_f32 v[66:67], v[192:193], v[82:83]
	v_pk_add_f32 v[68:69], v[190:191], v[84:85]
	v_pk_add_f32 v[66:67], v[86:87], v[66:67]
	v_pk_add_f32 v[68:69], v[88:89], v[68:69]
	v_pk_add_f32 v[130:131], v[90:91], v[66:67]
	v_pk_add_f32 v[132:133], v[92:93], v[68:69]
	s_waitcnt lgkmcnt(0)
; DI KParamsPtr kparams() { KParamsPtr p = (KParamsPtr)__builtin_amdgcn_kernarg_segment_ptr(); asm volatile("" : "+s"(p)); return p; }
; DI f32x16 mfma8(v8i a, v8i b, f32x16 c) { return __builtin_amdgcn_mfma_scale_f32_32x32x64_f8f6f4(a, b, c, 0, 0, 0, 0, 0, 0); }
; DI void attn_unit_a8(unsigned char* lds, const AttnArgs& a) {
;     ...
;     auto w_decode = [&](int j, const float*& src, unsigned char*& dst, int& ld, int& n0, int& k0, bool& gu) __attribute__((always_inline)) {
;         const int g = (j >> 2) * 512 + a.wl, e = g / 96, rr = g - e * 96; KParamsPtr kp = kparams();
;         if (rr < 64) { src = kp->w_gu + ((size_t)a.wli * NE + e) * (1024 * 2048); dst = kp->ws + WS_WGU + (size_t)a.wli * SZ_WGU + (size_t)e * 2048 * 1024; ld = 2048; n0 = (rr & 7) * 256; k0 = ((rr >> 3) * 4 + (j & 3)) * 32; gu = true; }
;         else { const int q = rr - 64; src = kp->w_dn + ((size_t)a.wli * NE + e) * (1024 * 1024); dst = kp->ws + WS_WDN + (size_t)a.wli * SZ_WDN + (size_t)e * 1024 * 1024; ld = 1024; n0 = (q & 3) * 256; k0 = ((q >> 2) * 4 + (j & 3)) * 32; gu = false; } };
; DI void attn_unit_d8(unsigned char* lds, const AttnArgs& a) {
;     ...
;     auto tile = [&](const unsigned char* Kb, const unsigned char* Kn, v8i& Pa, v8i& Pb, v8i& v0, v8i& v1, const v8i& Qa, const v8i& Qb, const v8i& w0, const v8i& w1) __attribute__((always_inline)) {
;         qk(Kb, 1, s1a, s1b);
;         v0 = rd32(Kb + voff); v1 = rd32(Kb + voff + 32 * A8_PITCH);
;         o0[0] = mfma8(w0, Qa, o0[0]); o1[0] = mfma8(w0, Qb, o1[0]); o0[1] = mfma8(w1, Qa, o0[1]); o1[1] = mfma8(w1, Qb, o1[1]);
;         expsum(s0a, l0); expsum(s0b, l1); pack4(s0a, Pa, 0); pack4(s0b, Pb, 0);
;         qk(Kn, 0, s0a, s0b);
;         expsum(s1a, l0); expsum(s1b, l1); pack4(s1a, Pa, 4); pack4(s1b, Pb, 4);
; #pragma unroll
;         for (int i = 0; i < 8; ++i) { __builtin_amdgcn_sched_group_barrier(0x008, 1, 0); __builtin_amdgcn_sched_group_barrier(0x402, 22, 0); }
;     };
	v_mfma_f32_32x32x64_f8f6f4 v[66:81], v[194:201], v[114:121], 0
	v_cvt_scalef32_pk_fp8_f32 v190, v98, v99, s36
	v_cvt_scalef32_pk_fp8_f32 v191, v102, v103, s36
	v_cvt_scalef32_pk_fp8_f32 v192, v106, v107, s36
	v_cvt_scalef32_pk_fp8_f32 v193, v110, v111, s36
	v_cvt_scalef32_pk_fp8_f32 v158, v82, v83, s36
	v_cvt_scalef32_pk_fp8_f32 v159, v86, v87, s36
	v_pk_add_f32 v[142:143], v[96:97], v[132:133]
	v_pk_add_f32 v[144:145], v[94:95], v[130:131]
	v_cvt_scalef32_pk_fp8_f32 v160, v90, v91, s36
	v_cvt_scalef32_pk_fp8_f32 v190, v100, v101, s36 op_sel:[0,0,0,1]
	v_cvt_scalef32_pk_fp8_f32 v191, v104, v105, s36 op_sel:[0,0,0,1]
	v_cvt_scalef32_pk_fp8_f32 v192, v108, v109, s36 op_sel:[0,0,0,1]
	v_cvt_scalef32_pk_fp8_f32 v193, v112, v113, s36 op_sel:[0,0,0,1]
	v_cvt_scalef32_pk_fp8_f32 v158, v84, v85, s36 op_sel:[0,0,0,1]
	v_cvt_scalef32_pk_fp8_f32 v159, v88, v89, s36 op_sel:[0,0,0,1]
	v_mfma_f32_32x32x64_f8f6f4 v[98:113], v[194:201], v[122:129], 0
	global_load_dwordx2 v[194:195], v[220:221], off
	global_load_dwordx2 v[196:197], v[222:223], off
	ds_read_b128 v[130:133], v234 offset:2560
	ds_read_b128 v[134:137], v234 offset:2576
	v_exp_f32_e32 v146, v66
	v_exp_f32_e32 v147, v67
	s_mulk_i32 s52, 0x2800
	s_add_i32 s8, s52, 0
	v_cvt_scalef32_pk_fp8_f32 v161, v94, v95, s36
	v_add_u32_e32 v224, s8, v183
	v_cvt_scalef32_pk_fp8_f32 v160, v92, v93, s36 op_sel:[0,0,0,1]
	v_cvt_scalef32_pk_fp8_f32 v161, v96, v97, s36 op_sel:[0,0,0,1]
	v_exp_f32_e32 v148, v68
	v_exp_f32_e32 v149, v69
	v_exp_f32_e32 v150, v70
	v_exp_f32_e32 v151, v71
	v_exp_f32_e32 v152, v72
	v_exp_f32_e32 v153, v73
	v_exp_f32_e32 v198, v74
	v_exp_f32_e32 v199, v75
	v_exp_f32_e32 v200, v76
	v_exp_f32_e32 v201, v77
	v_exp_f32_e32 v202, v78
	v_exp_f32_e32 v203, v79
	v_exp_f32_e32 v220, v80
	v_exp_f32_e32 v221, v81
	v_pk_add_f32 v[66:67], v[140:141], v[146:147]
	s_waitcnt lgkmcnt(0)
	v_mfma_f32_32x32x64_f8f6f4 v[82:97], v[130:137], v[114:121], 0
	v_add_f32_e64 v68, v138, v148
	v_add_f32_e64 v69, v139, v149
	v_add_f32_e64 v66, v150, v66
	v_add_f32_e64 v67, v151, v67
	v_add_f32_e64 v68, v152, v68
	v_add_f32_e64 v69, v153, v69
	v_add_f32_e64 v138, v198, v66
	v_add_f32_e64 v139, v199, v67
	v_add_f32_e64 v140, v200, v68
	v_add_f32_e64 v141, v201, v69
	v_exp_f32_e32 v98, v98
	v_exp_f32_e32 v99, v99
	v_exp_f32_e32 v100, v100
	v_exp_f32_e32 v101, v101
	v_exp_f32_e32 v102, v102
	v_exp_f32_e32 v103, v103
	v_exp_f32_e32 v104, v104
	v_exp_f32_e32 v105, v105
	v_exp_f32_e32 v106, v106
	v_exp_f32_e32 v107, v107
	v_exp_f32_e32 v108, v108
	v_exp_f32_e32 v109, v109
	v_exp_f32_e32 v110, v110
	v_exp_f32_e32 v111, v111
	v_exp_f32_e32 v112, v112
	v_exp_f32_e32 v113, v113
	v_exp_f32_e32 v82, v82
	v_mfma_f32_32x32x64_f8f6f4 v[66:81], v[130:137], v[122:129], 0
	v_add_f32_e64 v130, v144, v98
	v_add_f32_e64 v131, v145, v99
	v_add_f32_e64 v132, v142, v100
	v_add_f32_e64 v133, v143, v101
	v_add_f32_e64 v142, v102, v130
	v_add_f32_e64 v143, v103, v131
	v_add_f32_e64 v132, v104, v132
	v_add_f32_e64 v133, v105, v133
	v_add_f32_e64 v134, v220, v140
	v_add_f32_e64 v135, v221, v141
	v_add_f32_e64 v136, v202, v138
	v_add_f32_e64 v137, v203, v139
	v_pk_add_f32 v[142:143], v[106:107], v[142:143]
	v_pk_add_f32 v[132:133], v[108:109], v[132:133]
	v_cvt_scalef32_pk_fp8_f32 v138, v146, v147, s36
	v_cvt_scalef32_pk_fp8_f32 v139, v150, v151, s36
	v_cvt_scalef32_pk_fp8_f32 v140, v198, v199, s36
	v_cvt_scalef32_pk_fp8_f32 v141, v202, v203, s36
	v_cvt_scalef32_pk_fp8_f32 v130, v98, v99, s36
	v_cvt_scalef32_pk_fp8_f32 v131, v102, v103, s36
	v_pk_add_f32 v[146:147], v[112:113], v[132:133]
	v_pk_add_f32 v[150:151], v[110:111], v[142:143]
	v_mfma_f32_32x32x64_f8f6f4 v[50:65], v[170:177], v[186:193], v[50:65]
	v_exp_f32_e32 v83, v83
	v_exp_f32_e32 v84, v84
	v_exp_f32_e32 v85, v85
	v_add_u32_e32 v102, s50, v219
	v_exp_f32_e32 v86, v86
	v_exp_f32_e32 v87, v87
	v_exp_f32_e32 v88, v88
	v_exp_f32_e32 v89, v89
	v_cvt_scalef32_pk_fp8_f32 v130, v100, v101, s36 op_sel:[0,0,0,1]
	v_cvt_scalef32_pk_fp8_f32 v131, v104, v105, s36 op_sel:[0,0,0,1]
	v_exp_f32_e32 v90, v90
	v_exp_f32_e32 v91, v91
	v_exp_f32_e32 v92, v92
	v_exp_f32_e32 v93, v93
	ds_read_b128 v[98:101], v102
	ds_read_b128 v[102:105], v102 offset:16
	v_cvt_scalef32_pk_fp8_f32 v138, v148, v149, s36 op_sel:[0,0,0,1]
	v_cvt_scalef32_pk_fp8_f32 v139, v152, v153, s36 op_sel:[0,0,0,1]
	v_cvt_scalef32_pk_fp8_f32 v140, v200, v201, s36 op_sel:[0,0,0,1]
	v_cvt_scalef32_pk_fp8_f32 v141, v220, v221, s36 op_sel:[0,0,0,1]
	v_exp_f32_e32 v94, v94
	v_exp_f32_e32 v95, v95
	v_mfma_f32_32x32x64_f8f6f4 v[2:17], v[170:177], v[154:161], v[2:17]
	v_exp_f32_e32 v148, v96
	v_cvt_scalef32_pk_fp8_f32 v132, v106, v107, s36
	v_exp_f32_e32 v149, v97
	v_pk_add_f32 v[96:97], v[136:137], v[82:83]
; DI void attn_unit_a8(unsigned char* lds, const AttnArgs& a) {
;     ...
;     auto w_decode = [&](int j, const float*& src, unsigned char*& dst, int& ld, int& n0, int& k0, bool& gu) __attribute__((always_inline)) {
;         const int g = (j >> 2) * 512 + a.wl, e = g / 96, rr = g - e * 96; KParamsPtr kp = kparams();
;         if (rr < 64) { src = kp->w_gu + ((size_t)a.wli * NE + e) * (1024 * 2048); dst = kp->ws + WS_WGU + (size_t)a.wli * SZ_WGU + (size_t)e * 2048 * 1024; ld = 2048; n0 = (rr & 7) * 256; k0 = ((rr >> 3) * 4 + (j & 3)) * 32; gu = true; }
;         else { const int q = rr - 64; src = kp->w_dn + ((size_t)a.wli * NE + e) * (1024 * 1024); dst = kp->ws + WS_WDN + (size_t)a.wli * SZ_WDN + (size_t)e * 1024 * 1024; ld = 1024; n0 = (q & 3) * 256; k0 = ((q >> 2) * 4 + (j & 3)) * 32; gu = false; } };
;     auto w_issue = [&](int j) __attribute__((always_inline)) { const float* src; unsigned char* dst; int ld, n0, k0; bool gu; w_decode(j, src, dst, ld, n0, k0, gu);
;         const float* p = src + (size_t)(k0 + 4 * wid) * ld + n0 + wn4;
;         wq[0] = __builtin_nontemporal_load((const f32x4*)p); wq[1] = __builtin_nontemporal_load((const f32x4*)(p + ld));
;         wq[2] = __builtin_nontemporal_load((const f32x4*)(p + (size_t)2 * ld)); wq[3] = __builtin_nontemporal_load((const f32x4*)(p + (size_t)3 * ld)); };
;     auto w_cvt = [&]() __attribute__((always_inline)) { unsigned char* t8 = lds + AT_WT + wn4 * WPITCH + 4 * wid;
; #pragma unroll
;         for (int j = 0; j < 4; ++j) *(unsigned*)(t8 + j * WPITCH) = pk4_fp8_mul64(wq[0][j], wq[1][j], wq[2][j], wq[3][j]); };
;     const int wcol = tid >> 1, whalf = tid & 1;
;     const unsigned wper_gu = (unsigned)((wcol >> 7) * 256 + (wcol & 96) + invperm32(wcol & 31)) * 1024u + 16u * whalf;
;     const unsigned wper_dn = (unsigned)fwd_lane16(wcol) * 1024u + 16u * whalf;
;     auto w_store = [&](int j) __attribute__((always_inline)) { const float* src; unsigned char* dst; int ld, n0, k0; bool gu; w_decode(j, src, dst, ld, n0, k0, gu);
;         const int nb = n0 >> 8; const unsigned uni = (unsigned)(gu ? (nb & 3) * 512 + (nb >> 2) * 128 : nb * 256) * 1024u + (unsigned)k0;
;         const unsigned off = (gu ? wper_gu : wper_dn) + uni;
;         const unsigned* t = (const unsigned*)(lds + AT_WT + wcol * WPITCH + 16 * whalf);
;         *(u32x4*)(dst + off) = (u32x4){t[0], t[1], t[2], t[3]}; };
	v_pk_add_f32 v[106:107], v[134:135], v[84:85]
	v_exp_f32_e32 v66, v66
	v_exp_f32_e32 v67, v67
	v_exp_f32_e32 v68, v68
	v_exp_f32_e32 v69, v69
	v_cvt_scalef32_pk_fp8_f32 v133, v110, v111, s36
	v_pk_add_f32 v[106:107], v[88:89], v[106:107]
	v_pk_add_f32 v[96:97], v[86:87], v[96:97]
	v_exp_f32_e32 v70, v70
	v_exp_f32_e32 v71, v71
	v_exp_f32_e32 v72, v72
	v_exp_f32_e32 v73, v73
	v_cvt_scalef32_pk_fp8_f32 v132, v108, v109, s36 op_sel:[0,0,0,1]
	v_cvt_scalef32_pk_fp8_f32 v133, v112, v113, s36 op_sel:[0,0,0,1]
	v_pk_add_f32 v[96:97], v[90:91], v[96:97]
	v_pk_add_f32 v[106:107], v[92:93], v[106:107]
	v_exp_f32_e32 v74, v74
	v_exp_f32_e32 v75, v75
	v_mfma_f32_32x32x64_f8f6f4 v[34:49], v[162:169], v[186:193], v[34:49]
	v_exp_f32_e32 v76, v76
	v_exp_f32_e32 v77, v77
	v_exp_f32_e32 v78, v78
	v_exp_f32_e32 v79, v79
	v_exp_f32_e32 v80, v80
	v_exp_f32_e32 v81, v81
	v_cvt_scalef32_pk_fp8_f32 v142, v82, v83, s36
	v_cvt_scalef32_pk_fp8_f32 v143, v86, v87, s36
	v_cvt_scalef32_pk_fp8_f32 v144, v90, v91, s36
	v_cvt_scalef32_pk_fp8_f32 v142, v84, v85, s36 op_sel:[0,0,0,1]
	v_pk_add_f32 v[82:83], v[150:151], v[66:67]
	v_pk_add_f32 v[84:85], v[146:147], v[68:69]
	s_mulk_i32 s53, 0x2800
	v_pk_add_f32 v[186:187], v[148:149], v[106:107]
	v_pk_add_f32 v[188:189], v[94:95], v[96:97]
	v_cvt_scalef32_pk_fp8_f32 v145, v94, v95, s36
	v_cvt_scalef32_pk_fp8_f32 v143, v88, v89, s36 op_sel:[0,0,0,1]
	v_cvt_scalef32_pk_fp8_f32 v144, v92, v93, s36 op_sel:[0,0,0,1]
	v_pk_add_f32 v[84:85], v[72:73], v[84:85]
	v_mfma_f32_32x32x64_f8f6f4 v[18:33], v[162:169], v[154:161], v[18:33]
	v_add_f32_e64 v82, v70, v82
	v_add_f32_e64 v83, v71, v83
	s_add_i32 s51, s53, 0
	v_add_f32_e64 v82, v74, v82
	v_add_f32_e64 v83, v75, v83
	v_add_f32_e64 v84, v76, v84
	v_add_f32_e64 v85, v77, v85
	v_cvt_scalef32_pk_fp8_f32 v134, v66, v67, s36
	v_cvt_scalef32_pk_fp8_f32 v135, v70, v71, s36
	v_cvt_scalef32_pk_fp8_f32 v136, v74, v75, s36
	v_cvt_scalef32_pk_fp8_f32 v137, v78, v79, s36
	v_pk_add_f32 v[190:191], v[80:81], v[84:85]
	v_pk_add_f32 v[192:193], v[78:79], v[82:83]
	v_add_u32_e32 v106, s8, v218
	v_add_u32_e32 v107, s51, v183
	v_cvt_scalef32_pk_fp8_f32 v145, v148, v149, s36 op_sel:[0,0,0,1]
	v_cvt_scalef32_pk_fp8_f32 v134, v68, v69, s36 op_sel:[0,0,0,1]
	v_cvt_scalef32_pk_fp8_f32 v135, v72, v73, s36 op_sel:[0,0,0,1]
	v_cvt_scalef32_pk_fp8_f32 v136, v76, v77, s36 op_sel:[0,0,0,1]
	v_cvt_scalef32_pk_fp8_f32 v137, v80, v81, s36 op_sel:[0,0,0,1]
	s_waitcnt lgkmcnt(0)
	v_mfma_f32_32x32x64_f8f6f4 v[82:97], v[98:105], v[114:121], 0
	ds_read_b128 v[154:157], v234 offset:5120
	ds_read_b128 v[158:161], v234 offset:5136
	ds_read_b128 v[146:149], v234 offset:7680
	ds_read_b128 v[150:153], v234 offset:7696
	s_and_b32 s72, s61, 3
	s_cmp_eq_u32 s72, 0
	s_cbranch_scc0 .Lmy_rd1_nodec
	s_lshr_b32 s73, s61, 2
	s_lshl_b32 s73, s73, 9
	s_add_i32 s73, s73, s46
	s_mul_i32 s75, s73, 0xaaab
	s_lshr_b32 s75, s75, 22
	s_mul_i32 s76, s75, 0x60
	s_sub_i32 s76, s73, s76
	s_lshr_b32 s77, s76, 6
	s_lshl_b32 s78, s77, 6
	s_sub_i32 s76, s76, s78
	s_sub_i32 s78, 3, s77
	s_lshr_b32 s79, s76, s78
	s_lshl_b32 s79, s79, 2
	s_lshl_b32 s79, s79, 5
	s_lshl_b32 s81, s63, 2
	s_add_i32 s81, s81, s79
	s_sub_i32 s78, 13, s77
	s_lshl_b32 s81, s81, s78
	s_lshr_b32 s78, 7, s77
	s_and_b32 s78, s76, s78
	s_lshl_b32 s72, s78, 10
	s_add_i32 s81, s81, s72
	s_add_i32 s72, s75, 32
	s_sub_i32 s80, 23, s77
	s_lshl_b32 s72, s72, s80
	s_add_i32 s81, s81, s72
	s_cmp_eq_u32 s77, 0
	s_cselect_b64 s[84:85], s[66:67], s[68:69]
	s_add_u32 s84, s84, s81
	s_addc_u32 s85, s85, 0
	s_lshr_b32 s80, 0x2000, s77
	s_and_b32 s72, s78, 3
	s_lshl_b32 s72, s72, 19
	s_lshr_b32 s81, s78, 2
	s_lshl_b32 s81, s81, 17
	s_add_i32 s72, s72, s81
	s_lshl_b32 s81, s78, 18
	s_cmp_eq_u32 s77, 0
	s_cselect_b32 s72, s72, s81
	s_mul_i32 s81, s77, 0xc000000
	s_add_i32 s81, s81, 0x9094000
	s_add_i32 s72, s72, s79
	s_sub_i32 s73, 21, s77
	s_lshl_b32 s73, s75, s73
	s_add_i32 s72, s72, s73
	s_add_u32 s72, s72, s81
	s_or_b32 s79, s72, s77
.Lmy_rd1_nodec:
	s_cmpk_gt_i32 s46, 0x1ff
	s_cbranch_scc1 .Lmy_rd1_ldum
	s_add_i32 s72, s61, -1
	s_cmp_lt_u32 s72, 24
	s_cbranch_scc0 .Lmy_rd1_noc
	s_waitcnt vmcnt(4)
	v_cvt_scalef32_pk_fp8_f32 v236, v236, v240, s62
	v_cvt_scalef32_pk_fp8_f32 v237, v237, v241, s62
	v_cvt_scalef32_pk_fp8_f32 v238, v238, v242, s62
	v_cvt_scalef32_pk_fp8_f32 v239, v239, v243, s62
	v_cvt_scalef32_pk_fp8_f32 v236, v244, v248, s62 op_sel:[0,0,0,1]
	v_cvt_scalef32_pk_fp8_f32 v237, v245, v249, s62 op_sel:[0,0,0,1]
	v_cvt_scalef32_pk_fp8_f32 v238, v246, v250, s62 op_sel:[0,0,0,1]
	v_cvt_scalef32_pk_fp8_f32 v239, v247, v251, s62 op_sel:[0,0,0,1]
	ds_write_b32 v252, v236
	ds_write_b32 v252, v237 offset:36
	ds_write_b32 v252, v238 offset:72
	ds_write_b32 v252, v239 offset:108

; DI f32x16 mfma8(v8i a, v8i b, f32x16 c) { return __builtin_amdgcn_mfma_scale_f32_32x32x64_f8f6f4(a, b, c, 0, 0, 0, 0, 0, 0); }
; DI void attn_unit_a8(unsigned char* lds, const AttnArgs& a) {
;     ...
;     auto w_issue = [&](int j) __attribute__((always_inline)) { const float* src; unsigned char* dst; int ld, n0, k0; bool gu; w_decode(j, src, dst, ld, n0, k0, gu);
;         const float* p = src + (size_t)(k0 + 4 * wid) * ld + n0 + wn4;
;         wq[0] = __builtin_nontemporal_load((const f32x4*)p); wq[1] = __builtin_nontemporal_load((const f32x4*)(p + ld));
;         wq[2] = __builtin_nontemporal_load((const f32x4*)(p + (size_t)2 * ld)); wq[3] = __builtin_nontemporal_load((const f32x4*)(p + (size_t)3 * ld)); };
; DI void attn_unit_d8(unsigned char* lds, const AttnArgs& a) {
;     ...
;         lstore(s3, kreg0, vreg0); lstore(s4, kreg1, vreg1);
;         __syncthreads();
;         sb = s2;
;     }
;     o0[0] = mfma8(vY0, PaY, o0[0]); o1[0] = mfma8(vY0, PbY, o1[0]); o0[1] = mfma8(vY1, PaY, o0[1]); o1[1] = mfma8(vY1, PbY, o1[1]);
;     __builtin_amdgcn_s_setprio(0);
;     float lt0 = l0[0] + l0[1] + l0[2] + l0[3]; lt0 += __shfl_xor(lt0, 32);
;     float lt1 = l1[0] + l1[1] + l1[2] + l1[3]; lt1 += __shfl_xor(lt1, 32);
;     unsigned char* op = a.out8 + (size_t)(wid * 32 + r) * 1024 + 4 * h;
;     const float r0 = 16.0f / lt0, r1 = 16.0f * a.lam / lt1;
;     float ss = 0.f;
; #pragma unroll
;     for (int d = 0; d < 2; ++d)
; #pragma unroll
;         for (int i = 0; i < 16; ++i) { const float v = o0[d][i] * r0 - o1[d][i] * r1; o0[d][i] = v; ss += v * v; }
;     ss += __shfl_xor(ss, 32);
;     const float rinv = rsqrtf(ss * (1.0f / 64.0f) + EPS) * a.oscale * CAT_SCALE;
;     f32x4 ggv[2][4];
; #pragma unroll
;     for (int d = 0; d < 2; ++d)
; #pragma unroll
;         for (int g = 0; g < 4; ++g) ggv[d][g] = *(const f32x4*)(a.subg + 32 * d + 8 * g + 4 * h);
;     asm volatile("" : "+v"(ggv[0][0]), "+v"(ggv[1][3]));
.Lmy_rd1_lgo:
	global_load_dwordx4 v[236:239], v235, s[84:85] nt
	s_add_u32 s84, s84, s80
	s_addc_u32 s85, s85, 0
	global_load_dwordx4 v[240:243], v235, s[84:85] nt
	s_add_u32 s84, s84, s80
	s_addc_u32 s85, s85, 0
	global_load_dwordx4 v[244:247], v235, s[84:85] nt
	s_add_u32 s84, s84, s80
	s_addc_u32 s85, s85, 0
	global_load_dwordx4 v[248:251], v235, s[84:85] nt
	s_mov_b32 s65, s64
	s_mov_b32 s64, s79
	s_mul_i32 s72, s80, 29
	s_add_u32 s84, s84, s72
	s_addc_u32 s85, s85, 0
	s_add_i32 s79, s79, 32
	v_xor_b32_e32 v252, 0x4000, v252
	v_xor_b32_e32 v253, 0x4000, v253
	s_add_i32 s61, s61, 1
	s_cmpk_lt_u32 s22, 0x42
	s_waitcnt vmcnt(6)
	ds_write_b64 v224, v[194:195]
	v_mfma_f32_32x32x64_f8f6f4 v[66:81], v[98:105], v[122:129], 0
	v_add_u32_e32 v98, s51, v218
	v_add_u32_e32 v99, 0x1400, v106
	v_add_u32_e32 v98, 0x1400, v98
	ds_write2_b32 v99, v204, v205 offset1:8
	s_waitcnt vmcnt(5)
	ds_write_b64 v107, v[196:197]
	ds_write2_b32 v98, v206, v207 offset1:8
	s_waitcnt lgkmcnt(0)
	s_barrier
	s_cbranch_scc1 .LBB0_1888
	s_lshl_b64 s[16:17], s[16:17], 10
	s_add_u32 s8, s10, s16
	s_addc_u32 s17, s11, s17
	s_add_u32 s16, s8, s47
	v_mfma_f32_32x32x64_f8f6f4 v[50:65], v[154:161], v[138:145], v[50:65]
	s_addc_u32 s17, s17, 0
	v_mfma_f32_32x32x64_f8f6f4 v[2:17], v[154:161], v[130:137], v[2:17]
	v_mfma_f32_32x32x64_f8f6f4 v[34:49], v[146:153], v[138:145], v[34:49]
	v_mfma_f32_32x32x64_f8f6f4 v[18:33], v[146:153], v[130:137], v[18:33]
	s_setprio 0
	v_add_f32_e32 v66, v188, v189
	v_add_f32_e32 v66, v186, v66
	v_add_f32_e32 v66, v187, v66
	ds_bpermute_b32 v67, v1, v66
	v_add_f32_e32 v68, v192, v193
	v_add_f32_e32 v68, v190, v68
	v_add_f32_e32 v68, v191, v68
	ds_bpermute_b32 v69, v1, v68
	s_waitcnt lgkmcnt(1)
	v_add_f32_e32 v66, v66, v67
	v_div_scale_f32 v67, s[18:19], v66, v66, s36
	v_rcp_f32_e32 v70, v67
	s_waitcnt lgkmcnt(0)
	v_add_f32_e32 v68, v68, v69
	v_lshlrev_b32_e32 v178, 2, v217
	s_add_i32 s46, s46, s60
	v_fma_f32 v69, -v67, v70, 1.0
	v_fmac_f32_e32 v70, v69, v70
	v_div_scale_f32 v69, vcc, s36, v66, s36
	v_mul_f32_e32 v71, v69, v70
	v_fma_f32 v72, -v67, v71, v69
	v_fmac_f32_e32 v71, v72, v70
	v_fma_f32 v67, -v67, v71, v69
	v_div_scale_f32 v69, s[18:19], v68, v68, v214
	v_rcp_f32_e32 v72, v69
	v_div_fmas_f32 v67, v67, v70, v71
	v_div_fixup_f32 v66, v67, v66, s36
	s_cmpk_gt_i32 s46, 0x1ff
	v_fma_f32 v67, -v69, v72, 1.0
	v_fmac_f32_e32 v72, v67, v72
	v_div_scale_f32 v67, vcc, v214, v68, v214
	v_mul_f32_e32 v70, v67, v72
	v_fma_f32 v71, -v69, v70, v67
	v_fmac_f32_e32 v70, v71, v72
	v_fma_f32 v67, -v69, v70, v67
	v_div_fmas_f32 v67, v67, v72, v70
	v_div_fixup_f32 v68, v67, v68, v214
	v_mul_f32_e32 v2, v2, v68
	v_fma_f32 v50, v50, v66, -v2
	v_mul_f32_e32 v2, v3, v68
	v_fma_f32 v51, v51, v66, -v2
	v_mul_f32_e32 v67, v51, v51
	v_mul_f32_e32 v2, v4, v68
	v_fmac_f32_e32 v67, v50, v50
	v_fma_f32 v52, v52, v66, -v2
	v_mul_f32_e32 v2, v5, v68
	v_fmac_f32_e32 v67, v52, v52
	v_fma_f32 v53, v53, v66, -v2
	v_mul_f32_e32 v2, v6, v68
	v_fmac_f32_e32 v67, v53, v53
	v_fma_f32 v54, v54, v66, -v2
	v_mul_f32_e32 v2, v7, v68
	v_fmac_f32_e32 v67, v54, v54
	v_fma_f32 v55, v55, v66, -v2
	v_mul_f32_e32 v2, v8, v68
	v_fmac_f32_e32 v67, v55, v55
	v_fma_f32 v56, v56, v66, -v2
	v_mul_f32_e32 v2, v9, v68
	v_fmac_f32_e32 v67, v56, v56
	v_fma_f32 v57, v57, v66, -v2
	v_mul_f32_e32 v2, v10, v68
	v_fmac_f32_e32 v67, v57, v57
	v_fma_f32 v58, v58, v66, -v2
	v_mul_f32_e32 v2, v11, v68
	v_fmac_f32_e32 v67, v58, v58
	v_fma_f32 v59, v59, v66, -v2
	v_mul_f32_e32 v2, v12, v68
	v_fmac_f32_e32 v67, v59, v59
	v_fma_f32 v60, v60, v66, -v2
	v_mul_f32_e32 v2, v13, v68
	v_fmac_f32_e32 v67, v60, v60
	v_fma_f32 v61, v61, v66, -v2
	v_mul_f32_e32 v14, v14, v68
	v_fmac_f32_e32 v67, v61, v61
	v_fma_f32 v62, v62, v66, -v14
	v_mul_f32_e32 v14, v15, v68
	v_fmac_f32_e32 v67, v62, v62
	v_fma_f32 v63, v63, v66, -v14
	v_mul_f32_e32 v14, v16, v68
	v_lshlrev_b32_e32 v69, 4, v217
	v_fmac_f32_e32 v67, v63, v63
	v_fma_f32 v64, v64, v66, -v14
	v_mul_f32_e32 v14, v17, v68
	global_load_dwordx4 v[2:5], v69, s[12:13] offset:480
	global_load_dwordx4 v[6:9], v69, s[12:13] offset:288
	global_load_dwordx4 v[10:13], v69, s[12:13] offset:256
	v_fmac_f32_e32 v67, v64, v64
	v_fma_f32 v65, v65, v66, -v14
	v_mul_f32_e32 v14, v18, v68
	v_fmac_f32_e32 v67, v65, v65
	v_fma_f32 v70, v34, v66, -v14
	v_mul_f32_e32 v14, v19, v68
	v_fmac_f32_e32 v67, v70, v70
	v_fma_f32 v71, v35, v66, -v14
	v_mul_f32_e32 v14, v20, v68
	v_fmac_f32_e32 v67, v71, v71
	v_fma_f32 v72, v36, v66, -v14
	v_mul_f32_e32 v14, v21, v68
	v_fmac_f32_e32 v67, v72, v72
	v_fma_f32 v73, v37, v66, -v14
	v_mul_f32_e32 v14, v22, v68
	v_fmac_f32_e32 v67, v73, v73
	v_fma_f32 v74, v38, v66, -v14
	v_mul_f32_e32 v14, v23, v68
	v_fmac_f32_e32 v67, v74, v74
	v_fma_f32 v75, v39, v66, -v14
	v_fmac_f32_e32 v67, v75, v75
	v_pk_mul_f32 v[14:15], v[24:25], v[68:69] op_sel_hi:[1,0]
	v_pk_mul_f32 v[22:23], v[32:33], v[68:69] op_sel_hi:[1,0]
	v_pk_fma_f32 v[34:35], v[40:41], v[66:67], v[14:15] op_sel_hi:[1,0,1] neg_lo:[0,0,1] neg_hi:[0,0,1]
	s_nop 0
	v_pk_mul_f32 v[14:15], v[34:35], v[34:35]
	s_nop 0
	v_add_f32_e32 v14, v14, v67
	v_add_f32_e32 v20, v15, v14
	v_pk_mul_f32 v[14:15], v[26:27], v[68:69] op_sel_hi:[1,0]
	s_nop 0
	v_pk_fma_f32 v[36:37], v[42:43], v[66:67], v[14:15] op_sel_hi:[1,0,1] neg_lo:[0,0,1] neg_hi:[0,0,1]
	global_load_dwordx4 v[14:17], v69, s[12:13] offset:320
	v_pk_mul_f32 v[18:19], v[36:37], v[36:37]
	v_pk_fma_f32 v[42:43], v[48:49], v[66:67], v[22:23] op_sel_hi:[1,0,1] neg_lo:[0,0,1] neg_hi:[0,0,1]
	v_add_f32_e32 v18, v18, v20
	v_add_f32_e32 v20, v19, v18
	v_pk_mul_f32 v[18:19], v[28:29], v[68:69] op_sel_hi:[1,0]
	v_pk_mul_f32 v[22:23], v[42:43], v[42:43]
	v_pk_fma_f32 v[38:39], v[44:45], v[66:67], v[18:19] op_sel_hi:[1,0,1] neg_lo:[0,0,1] neg_hi:[0,0,1]
	s_nop 0
	v_pk_mul_f32 v[18:19], v[38:39], v[38:39]
	s_nop 0
	v_add_f32_e32 v18, v18, v20
	v_add_f32_e32 v20, v19, v18
	v_pk_mul_f32 v[18:19], v[30:31], v[68:69] op_sel_hi:[1,0]
	s_nop 0
	v_pk_fma_f32 v[40:41], v[46:47], v[66:67], v[18:19] op_sel_hi:[1,0,1] neg_lo:[0,0,1] neg_hi:[0,0,1]
	s_nop 0
	v_pk_mul_f32 v[18:19], v[40:41], v[40:41]
	s_nop 0
	v_add_f32_e32 v18, v18, v20
	v_add_f32_e32 v24, v19, v18
	v_add_f32_e32 v22, v22, v24
	v_add_f32_e32 v26, v23, v22
	ds_bpermute_b32 v27, v1, v26
	global_load_dwordx4 v[18:21], v69, s[12:13] offset:352
	global_load_dwordx4 v[22:25], v69, s[12:13] offset:448
	s_waitcnt lgkmcnt(0)
; DI unsigned pk4_fp8(float a, float b, float c, float d) { int r = 0; r = __builtin_amdgcn_cvt_pk_fp8_f32(a, b, r, false); r = __builtin_amdgcn_cvt_pk_fp8_f32(c, d, r, true); return (unsigned)r; }
; DI float clamp448(float x) { return __builtin_amdgcn_fmed3f(x, -448.0f, 448.0f); }
; DI void attn_unit_d8(unsigned char* lds, const AttnArgs& a) {
;     ...
;     ss += __shfl_xor(ss, 32);
;     const float rinv = rsqrtf(ss * (1.0f / 64.0f) + EPS) * a.oscale * CAT_SCALE;
;     f32x4 ggv[2][4];
; #pragma unroll
;     for (int d = 0; d < 2; ++d)
; #pragma unroll
;         for (int g = 0; g < 4; ++g) ggv[d][g] = *(const f32x4*)(a.subg + 32 * d + 8 * g + 4 * h);
;     asm volatile("" : "+v"(ggv[0][0]), "+v"(ggv[1][3]));
; #pragma unroll
;     for (int d = 0; d < 2; ++d)
; #pragma unroll
;         for (int g = 0; g < 4; ++g) { const f32x4 gg = ggv[d][g];
;             *(unsigned*)(op + 32 * d + 8 * g) = pk4_fp8(clamp448(o0[d][4 * g] * rinv * gg[0]), clamp448(o0[d][4 * g + 1] * rinv * gg[1]), clamp448(o0[d][4 * g + 2] * rinv * gg[2]), clamp448(o0[d][4 * g + 3] * rinv * gg[3])); }
	v_add_f32_e32 v26, v26, v27
	v_fmamk_f32 v26, v26, 0x3c800000, v215
	v_mul_f32_e32 v27, 0x4b800000, v26
	v_cmp_gt_f32_e32 vcc, s41, v26
	s_nop 1
	v_cndmask_b32_e32 v30, v26, v27, vcc
	global_load_dwordx4 v[26:29], v69, s[12:13] offset:384
	v_rsq_f32_e32 v32, v30
	v_lshlrev_b64 v[30:31], 10, v[180:181]
	v_lshl_add_u64 v[44:45], s[16:17], 0, v[30:31]
	v_lshl_add_u64 v[44:45], v[44:45], 0, v[178:179]
	v_mul_f32_e32 v30, 0x45800000, v32
	v_cndmask_b32_e32 v30, v32, v30, vcc
	v_mul_f32_e32 v48, v213, v30
	global_load_dwordx4 v[30:33], v69, s[12:13] offset:416
	v_mul_f32_e32 v48, 0x41800000, v48
	s_waitcnt vmcnt(5)
	v_mul_f32_e32 v49, v50, v48
	v_mul_f32_e32 v10, v10, v49
	v_mul_f32_e32 v49, v51, v48
	v_mul_f32_e32 v11, v11, v49
	v_mul_f32_e32 v49, v52, v48
	v_med3_f32 v10, v10, s42, v216
	v_med3_f32 v11, v11, s42, v216
	v_mul_f32_e32 v12, v12, v49
	s_nop 0
	v_cvt_pk_fp8_f32 v49, v10, v11
	v_mul_f32_e32 v10, v53, v48
	v_mul_f32_e32 v10, v13, v10
	v_med3_f32 v12, v12, s42, v216
	v_med3_f32 v10, v10, s42, v216
	v_cvt_pk_fp8_f32 v49, v12, v10 op_sel:[0,0,1]
	v_mul_f32_e32 v10, v54, v48
	v_mul_f32_e32 v6, v6, v10
	v_mul_f32_e32 v10, v55, v48
	v_mul_f32_e32 v7, v7, v10
	v_mul_f32_e32 v10, v56, v48
	v_med3_f32 v6, v6, s42, v216
	v_med3_f32 v7, v7, s42, v216
	v_mul_f32_e32 v8, v8, v10
	s_nop 0
	v_cvt_pk_fp8_f32 v10, v6, v7
	v_mul_f32_e32 v6, v57, v48
	v_mul_f32_e32 v6, v9, v6
	v_med3_f32 v8, v8, s42, v216
	v_med3_f32 v6, v6, s42, v216
	v_cvt_pk_fp8_f32 v10, v8, v6 op_sel:[0,0,1]
	v_add_co_u32_e32 v6, vcc, s43, v44
	v_lshl_add_u64 v[46:47], v[44:45], 0, s[14:15]
	s_nop 0
	v_addc_co_u32_e32 v7, vcc, 0, v45, vcc
	global_store_dword v[6:7], v49, off offset:768
	global_store_dword v[46:47], v10, off offset:8
	v_mul_f32_e32 v6, v58, v48
	v_mul_f32_e32 v7, v59, v48
	s_waitcnt vmcnt(6)
	v_mul_f32_e32 v6, v14, v6
	v_mul_f32_e32 v7, v15, v7
	v_med3_f32 v6, v6, s42, v216
	v_med3_f32 v7, v7, s42, v216
	s_nop 0
	v_cvt_pk_fp8_f32 v9, v6, v7
	v_mul_f32_e32 v8, v60, v48
	v_mul_f32_e32 v6, v61, v48
	v_mul_f32_e32 v8, v16, v8
	v_mul_f32_e32 v6, v17, v6
	v_med3_f32 v8, v8, s42, v216
	v_med3_f32 v6, v6, s42, v216
	v_cvt_pk_fp8_f32 v9, v8, v6 op_sel:[0,0,1]
	v_mul_f32_e32 v6, v62, v48
	v_mul_f32_e32 v7, v63, v48
	s_nop 0
	v_mul_f32_e32 v8, v64, v48
	s_nop 0
	s_waitcnt vmcnt(5)
	v_mul_f32_e32 v6, v18, v6
	v_mul_f32_e32 v7, v19, v7
	v_med3_f32 v6, v6, s42, v216
	v_med3_f32 v7, v7, s42, v216
	v_cvt_pk_fp8_f32 v10, v6, v7
	v_mul_f32_e32 v6, v65, v48
	v_mul_f32_e32 v8, v20, v8
	v_mul_f32_e32 v6, v21, v6
	v_med3_f32 v8, v8, s42, v216
	v_med3_f32 v6, v6, s42, v216
	v_cvt_pk_fp8_f32 v10, v8, v6 op_sel:[0,0,1]
	v_mul_f32_e32 v6, v70, v48
	v_mul_f32_e32 v7, v71, v48
	s_waitcnt vmcnt(3)
	v_mul_f32_e32 v6, v26, v6
	v_mul_f32_e32 v7, v27, v7
	v_med3_f32 v6, v6, s42, v216
	v_med3_f32 v7, v7, s42, v216
	v_cvt_pk_fp8_f32 v11, v6, v7
	v_mul_f32_e32 v8, v72, v48
	v_mul_f32_e32 v6, v73, v48
	v_mul_f32_e32 v8, v28, v8
	v_mul_f32_e32 v6, v29, v6
	v_med3_f32 v8, v8, s42, v216
	v_med3_f32 v6, v6, s42, v216
	v_cvt_pk_fp8_f32 v11, v8, v6 op_sel:[0,0,1]
	v_mul_f32_e32 v6, v74, v48
	v_mul_f32_e32 v7, v75, v48
	s_waitcnt vmcnt(2)
	v_mul_f32_e32 v6, v30, v6
	v_mul_f32_e32 v7, v31, v7
	v_med3_f32 v6, v6, s42, v216
	v_med3_f32 v7, v7, s42, v216
	s_nop 0
	v_cvt_pk_fp8_f32 v12, v6, v7
	v_mul_f32_e32 v8, v34, v48
	v_mul_f32_e32 v6, v35, v48
	v_mul_f32_e32 v8, v32, v8
	v_mul_f32_e32 v6, v33, v6
	v_med3_f32 v8, v8, s42, v216
	v_med3_f32 v6, v6, s42, v216
	v_cvt_pk_fp8_f32 v12, v8, v6 op_sel:[0,0,1]
	v_mul_f32_e32 v6, v36, v48
	v_mul_f32_e32 v7, v37, v48
	v_mul_f32_e32 v6, v22, v6
	v_mul_f32_e32 v7, v23, v7
	global_store_dword v[46:47], v9, off offset:16
	global_store_dword v[46:47], v10, off offset:24
	global_store_dword v[46:47], v11, off offset:32
	global_store_dword v[46:47], v12, off offset:40
	v_med3_f32 v6, v6, s42, v216
	v_med3_f32 v7, v7, s42, v216
	s_nop 0
	v_cvt_pk_fp8_f32 v9, v6, v7
	v_mul_f32_e32 v8, v38, v48
	v_mul_f32_e32 v6, v39, v48
	v_mul_f32_e32 v8, v24, v8
	v_mul_f32_e32 v6, v25, v6
	v_med3_f32 v8, v8, s42, v216
	v_med3_f32 v6, v6, s42, v216
	v_cvt_pk_fp8_f32 v9, v8, v6 op_sel:[0,0,1]
	v_mul_f32_e32 v6, v40, v48
	v_mul_f32_e32 v2, v2, v6
	v_mul_f32_e32 v6, v41, v48
	v_mul_f32_e32 v3, v3, v6
	v_mul_f32_e32 v6, v42, v48
	v_med3_f32 v2, v2, s42, v216
	v_med3_f32 v3, v3, s42, v216
	v_mul_f32_e32 v4, v4, v6
	s_nop 0
	v_cvt_pk_fp8_f32 v6, v2, v3
	v_mul_f32_e32 v2, v43, v48
	v_mul_f32_e32 v2, v5, v2
	v_med3_f32 v4, v4, s42, v216
	v_med3_f32 v2, v2, s42, v216
	v_cvt_pk_fp8_f32 v6, v4, v2 op_sel:[0,0,1]
	global_store_dword v[46:47], v9, off offset:48
	global_store_dword v[46:47], v6, off offset:56
	s_cbranch_scc0 .LBB0_1885
